# gate-merge epilogue br==2 path: z0/z1 tile loads of pieces 3-7 issued 1-2 pieces early into spare VGPRs, waits recomputed by simulation (on the SEL-optimised version, without the Y prefetch)
# baseline (speedup 1.0000x reference)
;     __device__ __forceinline__ void operator()(const f32x4 (&acc)[2][2][4][2], const Unit& u, int wr, int wc, int fr, int fq) const {
;     ...
;                 for (int bj = 0; bj < 2; ++bj) yv[m][bj] = *(const g_f16x8*)(Yb + offa + (size_t)m * 16 * 1024 + bj * HALF);
; #pragma unroll
;             for (int m = 2 * mp; m < 2 * mp + 2; ++m) { const size_t off = offa + (size_t)m * 16 * 1024;
;                 f16x8 za[2], zb[2];
;                 if (br == 2) {
; #pragma unroll
;                     for (int bj = 0; bj < 2; ++bj) { za[bj] = *(const g_f16x8*)(Y + off + bj * HALF); zb[bj] = *(const g_f16x8*)(Y + YSTR + off + bj * HALF); } }
;     ...
;                     f32x4 a0 = acc[ai][bj][m][0], a1 = acc[ai][bj][m][1];
;                     if constexpr (I8) { const i32x4 i0 = __builtin_bit_cast(i32x4, a0), i1 = __builtin_bit_cast(i32x4, a1);
;                         a0 = (f32x4){(float)i0.x, (float)i0.y, (float)i0.z, (float)i0.w} * sv[bj][0]; a1 = (f32x4){(float)i1.x, (float)i1.y, (float)i1.z, (float)i1.w} * sv[bj][1]; }
;                     const f32x4 g0 = a0 * rs[ai][m] + bv[bj][0], g1 = a1 * rs[ai][m] + bv[bj][1];
;                     const f16x8 yy = yv[m][bj];
;                     float z[8];
; #pragma unroll
;                     for (int e = 0; e < 4; ++e) { z[e] = (float)yy[e] * __builtin_amdgcn_rcpf(1.f + __builtin_amdgcn_exp2f(-LOG2E * g0[e])); z[4 + e] = (float)yy[4 + e] * __builtin_amdgcn_rcpf(1.f + __builtin_amdgcn_exp2f(-LOG2E * g1[e])); }
;                     if (br == 2) {
; #pragma unroll
;                         for (int e = 0; e < 8; ++e) z[e] += (float)za[bj][e] + (float)zb[bj][e]; }
.LBB0_1247:
	s_mov_b64 s[28:29], 0x8000
	v_lshl_add_u64 v[158:159], v[178:179], 0, s[28:29]
	v_cvt_pk_f16_f32 v154, v146, v147
	v_cvt_pk_f16_f32 v155, v152, v153
	v_cvt_pk_f16_f32 v156, v150, v151
	v_cvt_pk_f16_f32 v157, v148, v149
	v_add_co_u32_e32 v146, vcc, 0x10000, v224
	global_store_dwordx4 v[158:159], v[154:157], off offset:256
	s_nop 0
	v_addc_co_u32_e32 v147, vcc, 0, v225, vcc
	global_load_dwordx4 v[158:161], v[146:147], off
	global_load_dwordx4 v[154:157], v[146:147], off offset:256
	v_add_co_u32_e32 v146, vcc, 0x18000, v224
	s_nop 1
	v_addc_co_u32_e32 v147, vcc, 0, v225, vcc
	global_load_dwordx4 v[150:153], v[146:147], off
	s_nop 0
	global_load_dwordx4 v[146:149], v[146:147], off offset:256
	s_and_b64 vcc, exec, s[36:37]
	s_cbranch_vccnz .LBB0_1249
	v_mov_b64_e32 v[42:43], 0x10000
	v_lshl_add_u64 v[42:43], v[228:229], 1, v[42:43]
	v_lshl_add_u64 v[44:45], s[40:41], 0, v[42:43]
	s_waitcnt vmcnt(6)
	v_lshl_add_u64 v[46:47], s[44:45], 0, v[42:43]
	global_load_dwordx4 v[58:61], v[44:45], off
	s_nop 0
	global_load_dwordx4 v[42:45], v[44:45], off offset:256
	s_nop 0
	global_load_dwordx4 v[66:69], v[46:47], off
	s_nop 0
	global_load_dwordx4 v[46:49], v[46:47], off offset:256
	s_mov_b64 s[28:29], 0x18000
	v_lshl_add_u64 v[180:181], v[228:229], 1, s[28:29]
	v_lshl_add_u64 v[246:247], s[44:45], 0, v[180:181]
	v_lshl_add_u64 v[180:181], s[40:41], 0, v[180:181]
	global_load_dwordx4 v[174:177], v[180:181], off
	global_load_dwordx4 v[180:183], v[180:181], off offset:256
	global_load_dwordx4 v[238:241], v[246:247], off
	global_load_dwordx4 v[246:249], v[246:247], off offset:256
.LBB0_1249:
	v_cvt_f32_i32_e32 v162, v138
	v_cvt_f32_i32_e32 v163, v139
	v_cvt_f32_i32_e32 v142, v142
	v_cvt_f32_i32_e32 v143, v143
	v_mul_f32_e32 v139, v54, v162
	v_fma_f32 v139, v220, v139, v50
	v_mul_f32_e32 v139, 0xbfb8aa3b, v139
	v_exp_f32_e32 v139, v139
	v_cvt_f32_i32_e32 v164, v140
	v_mul_f32_e32 v138, v70, v142
	v_fma_f32 v138, v220, v138, v62
	v_add_f32_e32 v139, 1.0, v139
	v_rcp_f32_e32 v140, v139
	v_mul_f32_e32 v139, v71, v143
	v_fma_f32 v139, v220, v139, v63
	v_mul_f32_e32 v138, 0xbfb8aa3b, v138
	v_mul_f32_e32 v139, 0xbfb8aa3b, v139
	v_exp_f32_e32 v138, v138
	v_exp_f32_e32 v139, v139
	v_cvt_f32_i32_e32 v165, v141
	v_mul_f32_e32 v141, v55, v163
	v_fma_f32 v141, v220, v141, v51
	v_mul_f32_e32 v141, 0xbfb8aa3b, v141
	v_add_f32_e32 v138, 1.0, v138
	v_add_f32_e32 v139, 1.0, v139
	v_exp_f32_e32 v141, v141
	v_rcp_f32_e32 v138, v138
	v_rcp_f32_e32 v139, v139
	s_cmp_lg_u64 s[36:37], 0
	s_cbranch_scc0 .Lg3w_30804
	s_waitcnt vmcnt(3)
	s_branch .Lg3j_30804
.Lg3w_30804:
	s_waitcnt vmcnt(7)
.Lg3j_30804:
	v_cvt_f32_f16_sdwa v143, v158 dst_sel:DWORD dst_unused:UNUSED_PAD src0_sel:WORD_1
	v_cvt_f32_f16_e32 v142, v158
	v_add_f32_e32 v141, 1.0, v141
	v_rcp_f32_e32 v141, v141
	v_cvt_f32_i32_e32 v144, v144
	v_pk_mul_f32 v[138:139], v[138:139], v[142:143]
	v_cvt_f32_f16_sdwa v143, v160 dst_sel:DWORD dst_unused:UNUSED_PAD src0_sel:WORD_1
	v_cvt_f32_f16_e32 v142, v160
	v_cvt_f32_i32_e32 v145, v145
	v_cvt_f32_f16_sdwa v163, v159 dst_sel:DWORD dst_unused:UNUSED_PAD src0_sel:WORD_1
	v_cvt_f32_f16_e32 v162, v159
	v_pk_mul_f32 v[140:141], v[140:141], v[142:143]
	v_mul_f32_e32 v143, v56, v164
	v_fma_f32 v143, v220, v143, v52
	v_mul_f32_e32 v143, 0xbfb8aa3b, v143
	v_exp_f32_e32 v143, v143
	v_mul_f32_e32 v142, v72, v144
	v_fma_f32 v142, v220, v142, v64
	v_mul_f32_e32 v142, 0xbfb8aa3b, v142
	v_add_f32_e32 v143, 1.0, v143
	v_rcp_f32_e32 v144, v143
	v_mul_f32_e32 v143, v73, v145
	v_mul_f32_e32 v145, v57, v165
	v_fma_f32 v143, v220, v143, v65
	v_fma_f32 v145, v220, v145, v53
	v_mul_f32_e32 v143, 0xbfb8aa3b, v143
	v_mul_f32_e32 v145, 0xbfb8aa3b, v145
	v_exp_f32_e32 v142, v142
	v_exp_f32_e32 v143, v143
	v_exp_f32_e32 v145, v145
	v_cvt_f32_f16_sdwa v159, v161 dst_sel:DWORD dst_unused:UNUSED_PAD src0_sel:WORD_1
	v_add_f32_e32 v142, 1.0, v142
	v_add_f32_e32 v143, 1.0, v143
	v_add_f32_e32 v145, 1.0, v145
	v_rcp_f32_e32 v142, v142
	v_rcp_f32_e32 v143, v143
	v_rcp_f32_e32 v145, v145
	v_cvt_f32_f16_e32 v158, v161
	s_and_b64 vcc, exec, s[36:37]
	v_pk_mul_f32 v[142:143], v[142:143], v[162:163]
	v_pk_mul_f32 v[144:145], v[144:145], v[158:159]
	s_cbranch_vccnz .LBB0_1251
	v_cvt_f32_f16_sdwa v159, v58 dst_sel:DWORD dst_unused:UNUSED_PAD src0_sel:WORD_1
	v_cvt_f32_f16_e32 v158, v58
	s_waitcnt vmcnt(5)
	v_cvt_f32_f16_sdwa v161, v66 dst_sel:DWORD dst_unused:UNUSED_PAD src0_sel:WORD_1
	v_cvt_f32_f16_e32 v160, v66
	v_cvt_f32_f16_sdwa v163, v59 dst_sel:DWORD dst_unused:UNUSED_PAD src0_sel:WORD_1
	v_cvt_f32_f16_e32 v162, v59
	v_cvt_f32_f16_sdwa v165, v67 dst_sel:DWORD dst_unused:UNUSED_PAD src0_sel:WORD_1
	v_cvt_f32_f16_e32 v164, v67
	v_cvt_f32_f16_sdwa v167, v60 dst_sel:DWORD dst_unused:UNUSED_PAD src0_sel:WORD_1
	v_cvt_f32_f16_e32 v166, v60
	v_cvt_f32_f16_sdwa v169, v68 dst_sel:DWORD dst_unused:UNUSED_PAD src0_sel:WORD_1
	v_cvt_f32_f16_e32 v168, v68
	v_cvt_f32_f16_sdwa v171, v61 dst_sel:DWORD dst_unused:UNUSED_PAD src0_sel:WORD_1
	v_cvt_f32_f16_e32 v170, v61
	v_cvt_f32_f16_sdwa v173, v69 dst_sel:DWORD dst_unused:UNUSED_PAD src0_sel:WORD_1
	v_cvt_f32_f16_e32 v172, v69
	v_pk_add_f32 v[158:159], v[160:161], v[158:159]
	v_pk_add_f32 v[160:161], v[164:165], v[162:163]
	v_pk_add_f32 v[162:163], v[168:169], v[166:167]
	v_pk_add_f32 v[164:165], v[172:173], v[170:171]
	v_pk_add_f32 v[138:139], v[138:139], v[158:159]
	v_pk_add_f32 v[142:143], v[142:143], v[160:161]
	v_pk_add_f32 v[140:141], v[140:141], v[162:163]
	v_pk_add_f32 v[144:145], v[144:145], v[164:165]
.LBB0_1251:
	s_mov_b32 s26, 0x10000
	v_cvt_pk_f16_f32 v138, v138, v139
	v_cvt_pk_f16_f32 v139, v142, v143
	v_add_co_u32_e32 v142, vcc, s26, v178
	v_cvt_pk_f16_f32 v140, v140, v141
	v_cvt_pk_f16_f32 v141, v144, v145
	v_addc_co_u32_e32 v143, vcc, 0, v179, vcc
	global_store_dwordx4 v[142:143], v[138:141], off
	v_cvt_f32_i32_e32 v134, v134
	v_cvt_f32_i32_e32 v135, v135
	v_cvt_f32_i32_e32 v138, v136
	v_cvt_f32_i32_e32 v136, v130
	v_cvt_f32_i32_e32 v140, v131
	v_mul_f32_e32 v130, v38, v134
	v_fma_f32 v130, v220, v130, v34
	v_mul_f32_e32 v131, v30, v136
	v_fma_f32 v131, v220, v131, v26
	v_mul_f32_e32 v131, 0xbfb8aa3b, v131
	v_exp_f32_e32 v131, v131
	v_mul_f32_e32 v130, 0xbfb8aa3b, v130
	v_exp_f32_e32 v130, v130
	v_cvt_f32_i32_e32 v139, v137
	v_add_f32_e32 v131, 1.0, v131
	v_rcp_f32_e32 v134, v131
	v_mul_f32_e32 v131, v39, v135
	v_fma_f32 v131, v220, v131, v35
	v_mul_f32_e32 v131, 0xbfb8aa3b, v131
	v_exp_f32_e32 v131, v131
	v_mul_f32_e32 v135, v31, v140
	v_fma_f32 v135, v220, v135, v27
	v_mul_f32_e32 v135, 0xbfb8aa3b, v135
	v_add_f32_e32 v130, 1.0, v130
	v_add_f32_e32 v131, 1.0, v131
	v_exp_f32_e32 v135, v135
	v_rcp_f32_e32 v130, v130
	v_rcp_f32_e32 v131, v131
	s_cmp_lg_u64 s[36:37], 0
	s_cbranch_scc0 .Lg3w_30910
	s_waitcnt vmcnt(3)
	s_branch .Lg3j_30910

; __device__ __forceinline__ unsigned pk2h(float lo, float hi) { f32x2 v = {lo, hi}; f16x2 h = __builtin_convertvector(v, f16x2); return __builtin_bit_cast(unsigned, h); }
;     __device__ __forceinline__ void operator()(const f32x4 (&acc)[2][2][4][2], const Unit& u, int wr, int wc, int fr, int fq) const {
;     ...
;                 for (int bj = 0; bj < 2; ++bj) yv[m][bj] = *(const g_f16x8*)(Yb + offa + (size_t)m * 16 * 1024 + bj * HALF);
; #pragma unroll
;             for (int m = 2 * mp; m < 2 * mp + 2; ++m) { const size_t off = offa + (size_t)m * 16 * 1024;
;                 f16x8 za[2], zb[2];
;                 if (br == 2) {
; #pragma unroll
;                     for (int bj = 0; bj < 2; ++bj) { za[bj] = *(const g_f16x8*)(Y + off + bj * HALF); zb[bj] = *(const g_f16x8*)(Y + YSTR + off + bj * HALF); } }
; #pragma unroll
;                 for (int bj = 0; bj < 2; ++bj) {
;                     f32x4 a0 = acc[ai][bj][m][0], a1 = acc[ai][bj][m][1];
;                     if constexpr (I8) { const i32x4 i0 = __builtin_bit_cast(i32x4, a0), i1 = __builtin_bit_cast(i32x4, a1);
;                         a0 = (f32x4){(float)i0.x, (float)i0.y, (float)i0.z, (float)i0.w} * sv[bj][0]; a1 = (f32x4){(float)i1.x, (float)i1.y, (float)i1.z, (float)i1.w} * sv[bj][1]; }
;                     const f32x4 g0 = a0 * rs[ai][m] + bv[bj][0], g1 = a1 * rs[ai][m] + bv[bj][1];
;                     const f16x8 yy = yv[m][bj];
;                     float z[8];
; #pragma unroll
;                     for (int e = 0; e < 4; ++e) { z[e] = (float)yy[e] * __builtin_amdgcn_rcpf(1.f + __builtin_amdgcn_exp2f(-LOG2E * g0[e])); z[4 + e] = (float)yy[4 + e] * __builtin_amdgcn_rcpf(1.f + __builtin_amdgcn_exp2f(-LOG2E * g1[e])); }
;                     if (br == 2) {
; #pragma unroll
;                         for (int e = 0; e < 8; ++e) z[e] += (float)za[bj][e] + (float)zb[bj][e]; }
;                     u32x4 w; w.x = pk2h(z[0], z[1]); w.y = pk2h(z[2], z[3]); w.z = pk2h(z[4], z[5]); w.w = pk2h(z[6], z[7]);
;                     f16* dst = (br == 2) ? merged : Yb;
;                     gst16(dst + off + bj * HALF, w); } } } }
.Lg3j_30910:
	v_cvt_f32_f16_sdwa v137, v154 dst_sel:DWORD dst_unused:UNUSED_PAD src0_sel:WORD_1
	v_cvt_f32_f16_e32 v136, v154
	v_add_f32_e32 v135, 1.0, v135
	v_rcp_f32_e32 v135, v135
	s_mov_b64 s[50:51], -1
	v_pk_mul_f32 v[130:131], v[130:131], v[136:137]
	v_cvt_f32_f16_sdwa v137, v156 dst_sel:DWORD dst_unused:UNUSED_PAD src0_sel:WORD_1
	v_cvt_f32_f16_e32 v136, v156
	s_and_b64 vcc, exec, s[38:39]
	v_pk_mul_f32 v[134:135], v[134:135], v[136:137]
	v_mul_f32_e32 v136, v40, v138
	v_mul_f32_e32 v137, v41, v139
	v_fma_f32 v136, v220, v136, v36
	v_fma_f32 v137, v220, v137, v37
	v_mul_f32_e32 v136, 0xbfb8aa3b, v136
	v_mul_f32_e32 v137, 0xbfb8aa3b, v137
	v_exp_f32_e32 v136, v136
	v_exp_f32_e32 v137, v137
	v_cvt_f32_f16_sdwa v139, v155 dst_sel:DWORD dst_unused:UNUSED_PAD src0_sel:WORD_1
	v_cvt_f32_f16_e32 v138, v155
	v_add_f32_e32 v136, 1.0, v136
	v_add_f32_e32 v137, 1.0, v137
	v_rcp_f32_e32 v136, v136
	v_rcp_f32_e32 v137, v137
	s_nop 0
	v_pk_mul_f32 v[136:137], v[136:137], v[138:139]
	s_cbranch_vccnz .LBB0_1253
	s_mov_b64 s[50:51], 0
.LBB0_1253:
	v_cvt_f32_i32_e32 v132, v132
	v_cvt_f32_i32_e32 v133, v133
	v_cvt_f32_f16_sdwa v139, v157 dst_sel:DWORD dst_unused:UNUSED_PAD src0_sel:WORD_1
	v_cvt_f32_f16_e32 v138, v157
	v_mul_f32_e32 v132, v32, v132
	v_mul_f32_e32 v133, v33, v133
	v_fma_f32 v132, v220, v132, v28
	v_fma_f32 v133, v220, v133, v29
	v_mul_f32_e32 v132, 0xbfb8aa3b, v132
	v_mul_f32_e32 v133, 0xbfb8aa3b, v133
	v_exp_f32_e32 v132, v132
	v_exp_f32_e32 v133, v133
	s_andn2_b64 vcc, exec, s[50:51]
	v_add_f32_e32 v132, 1.0, v132
	v_add_f32_e32 v133, 1.0, v133
	v_rcp_f32_e32 v132, v132
	v_rcp_f32_e32 v133, v133
	s_nop 0
	v_pk_mul_f32 v[132:133], v[132:133], v[138:139]
	s_cbranch_vccnz .LBB0_1255
	v_cvt_f32_f16_sdwa v139, v42 dst_sel:DWORD dst_unused:UNUSED_PAD src0_sel:WORD_1
	v_cvt_f32_f16_e32 v138, v42
	s_waitcnt vmcnt(5)
	v_cvt_f32_f16_sdwa v141, v46 dst_sel:DWORD dst_unused:UNUSED_PAD src0_sel:WORD_1
	v_cvt_f32_f16_e32 v140, v46
	v_cvt_f32_f16_sdwa v143, v43 dst_sel:DWORD dst_unused:UNUSED_PAD src0_sel:WORD_1
	v_cvt_f32_f16_e32 v142, v43
	v_cvt_f32_f16_sdwa v145, v47 dst_sel:DWORD dst_unused:UNUSED_PAD src0_sel:WORD_1
	v_cvt_f32_f16_e32 v144, v47
	v_cvt_f32_f16_sdwa v155, v44 dst_sel:DWORD dst_unused:UNUSED_PAD src0_sel:WORD_1
	v_cvt_f32_f16_e32 v154, v44
	v_cvt_f32_f16_sdwa v157, v48 dst_sel:DWORD dst_unused:UNUSED_PAD src0_sel:WORD_1
	v_cvt_f32_f16_e32 v156, v48
	v_cvt_f32_f16_sdwa v159, v45 dst_sel:DWORD dst_unused:UNUSED_PAD src0_sel:WORD_1
	v_cvt_f32_f16_e32 v158, v45
	v_cvt_f32_f16_sdwa v161, v49 dst_sel:DWORD dst_unused:UNUSED_PAD src0_sel:WORD_1
	v_cvt_f32_f16_e32 v160, v49
	v_pk_add_f32 v[138:139], v[140:141], v[138:139]
	v_pk_add_f32 v[140:141], v[144:145], v[142:143]
	v_pk_add_f32 v[142:143], v[156:157], v[154:155]
	v_pk_add_f32 v[144:145], v[160:161], v[158:159]
	v_pk_add_f32 v[130:131], v[130:131], v[138:139]
	v_pk_add_f32 v[136:137], v[136:137], v[140:141]
	v_pk_add_f32 v[134:135], v[134:135], v[142:143]
	v_pk_add_f32 v[132:133], v[132:133], v[144:145]
.LBB0_1255:
	s_mov_b64 s[28:29], 0x10000
	v_lshl_add_u64 v[142:143], v[178:179], 0, s[28:29]
	v_cvt_pk_f16_f32 v138, v130, v131
	v_cvt_pk_f16_f32 v139, v136, v137
	v_cvt_pk_f16_f32 v140, v134, v135
	v_cvt_pk_f16_f32 v141, v132, v133
	s_and_b64 vcc, exec, s[36:37]
	global_store_dwordx4 v[142:143], v[138:141], off offset:256
	s_cbranch_vccnz .LBB0_1257
	v_mov_b64_e32 v[42:43], 0x18000
	v_lshl_add_u64 v[42:43], v[228:229], 1, v[42:43]
	v_lshl_add_u64 v[44:45], s[40:41], 0, v[42:43]
	s_waitcnt vmcnt(6)
	v_lshl_add_u64 v[46:47], s[44:45], 0, v[42:43]
	s_nop 0
	s_nop 0
	s_nop 0
	s_mov_b64 s[28:29], 0x40000
	v_lshl_add_u64 v[158:159], v[228:229], 1, s[28:29]
	v_lshl_add_u64 v[166:167], s[44:45], 0, v[158:159]
	v_lshl_add_u64 v[158:159], s[40:41], 0, v[158:159]
	global_load_dwordx4 v[154:157], v[158:159], off
	global_load_dwordx4 v[158:161], v[158:159], off offset:256
	global_load_dwordx4 v[162:165], v[166:167], off
	global_load_dwordx4 v[166:169], v[166:167], off offset:256
.LBB0_1257:
	v_cvt_f32_i32_e32 v130, v122
	v_cvt_f32_i32_e32 v131, v123
	v_cvt_f32_i32_e32 v126, v126
	v_cvt_f32_i32_e32 v127, v127
	v_mul_f32_e32 v123, v54, v130
	v_fma_f32 v123, v221, v123, v50
	v_mul_f32_e32 v123, 0xbfb8aa3b, v123
	v_exp_f32_e32 v123, v123
	v_cvt_f32_i32_e32 v132, v124
	v_mul_f32_e32 v122, v70, v126
	v_fma_f32 v122, v221, v122, v62
	v_add_f32_e32 v123, 1.0, v123
	v_rcp_f32_e32 v124, v123
	v_mul_f32_e32 v123, v71, v127
	v_fma_f32 v123, v221, v123, v63
	v_mul_f32_e32 v122, 0xbfb8aa3b, v122
	v_mul_f32_e32 v123, 0xbfb8aa3b, v123
	v_exp_f32_e32 v122, v122
	v_exp_f32_e32 v123, v123
	v_cvt_f32_i32_e32 v133, v125
	v_mul_f32_e32 v125, v55, v131
	v_fma_f32 v125, v221, v125, v51
	v_mul_f32_e32 v125, 0xbfb8aa3b, v125
	v_add_f32_e32 v122, 1.0, v122
	v_add_f32_e32 v123, 1.0, v123
	v_exp_f32_e32 v125, v125
	v_rcp_f32_e32 v122, v122
	v_rcp_f32_e32 v123, v123
	s_cmp_lg_u64 s[36:37], 0
	s_cbranch_scc0 .Lg3w_31039
	s_waitcnt vmcnt(3)
	s_branch .Lg3j_31039
; __device__ __forceinline__ unsigned pk2h(float lo, float hi) { f32x2 v = {lo, hi}; f16x2 h = __builtin_convertvector(v, f16x2); return __builtin_bit_cast(unsigned, h); }
;     __device__ __forceinline__ void operator()(const f32x4 (&acc)[2][2][4][2], const Unit& u, int wr, int wc, int fr, int fq) const {
;     ...
;                     f32x4 a0 = acc[ai][bj][m][0], a1 = acc[ai][bj][m][1];
;                     if constexpr (I8) { const i32x4 i0 = __builtin_bit_cast(i32x4, a0), i1 = __builtin_bit_cast(i32x4, a1);
;                         a0 = (f32x4){(float)i0.x, (float)i0.y, (float)i0.z, (float)i0.w} * sv[bj][0]; a1 = (f32x4){(float)i1.x, (float)i1.y, (float)i1.z, (float)i1.w} * sv[bj][1]; }
;                     const f32x4 g0 = a0 * rs[ai][m] + bv[bj][0], g1 = a1 * rs[ai][m] + bv[bj][1];
;                     const f16x8 yy = yv[m][bj];
;                     float z[8];
; #pragma unroll
;                     for (int e = 0; e < 4; ++e) { z[e] = (float)yy[e] * __builtin_amdgcn_rcpf(1.f + __builtin_amdgcn_exp2f(-LOG2E * g0[e])); z[4 + e] = (float)yy[4 + e] * __builtin_amdgcn_rcpf(1.f + __builtin_amdgcn_exp2f(-LOG2E * g1[e])); }
;                     if (br == 2) {
; #pragma unroll
;                         for (int e = 0; e < 8; ++e) z[e] += (float)za[bj][e] + (float)zb[bj][e]; }
;                     u32x4 w; w.x = pk2h(z[0], z[1]); w.y = pk2h(z[2], z[3]); w.z = pk2h(z[4], z[5]); w.w = pk2h(z[6], z[7]);
;                     f16* dst = (br == 2) ? merged : Yb;
;                     gst16(dst + off + bj * HALF, w); } } } }
.Lg3w_31039:
	s_waitcnt vmcnt(9)
.Lg3j_31039:
	v_cvt_f32_f16_sdwa v127, v150 dst_sel:DWORD dst_unused:UNUSED_PAD src0_sel:WORD_1
	v_cvt_f32_f16_e32 v126, v150
	v_add_f32_e32 v125, 1.0, v125
	v_rcp_f32_e32 v125, v125
	v_cvt_f32_i32_e32 v128, v128
	v_pk_mul_f32 v[122:123], v[122:123], v[126:127]
	v_cvt_f32_f16_sdwa v127, v152 dst_sel:DWORD dst_unused:UNUSED_PAD src0_sel:WORD_1
	v_cvt_f32_f16_e32 v126, v152
	v_cvt_f32_i32_e32 v129, v129
	v_cvt_f32_f16_sdwa v131, v151 dst_sel:DWORD dst_unused:UNUSED_PAD src0_sel:WORD_1
	v_cvt_f32_f16_e32 v130, v151
	v_pk_mul_f32 v[124:125], v[124:125], v[126:127]
	v_mul_f32_e32 v127, v56, v132
	v_fma_f32 v127, v221, v127, v52
	v_mul_f32_e32 v127, 0xbfb8aa3b, v127
	v_exp_f32_e32 v127, v127
	v_mul_f32_e32 v126, v72, v128
	v_fma_f32 v126, v221, v126, v64
	v_mul_f32_e32 v126, 0xbfb8aa3b, v126
	v_add_f32_e32 v127, 1.0, v127
	v_rcp_f32_e32 v128, v127
	v_mul_f32_e32 v127, v73, v129
	v_fma_f32 v127, v221, v127, v65
	v_mul_f32_e32 v127, 0xbfb8aa3b, v127
	v_exp_f32_e32 v126, v126
	v_exp_f32_e32 v127, v127
	v_mul_f32_e32 v129, v57, v133
	v_fma_f32 v129, v221, v129, v53
	v_mul_f32_e32 v129, 0xbfb8aa3b, v129
	v_add_f32_e32 v126, 1.0, v126
	v_add_f32_e32 v127, 1.0, v127
	v_exp_f32_e32 v129, v129
	v_rcp_f32_e32 v126, v126
	v_rcp_f32_e32 v127, v127
	s_and_b64 vcc, exec, s[36:37]
	v_add_f32_e32 v129, 1.0, v129
	v_rcp_f32_e32 v129, v129
	v_pk_mul_f32 v[126:127], v[126:127], v[130:131]
	v_cvt_f32_f16_sdwa v131, v153 dst_sel:DWORD dst_unused:UNUSED_PAD src0_sel:WORD_1
	v_cvt_f32_f16_e32 v130, v153
	v_pk_mul_f32 v[128:129], v[128:129], v[130:131]
	s_cbranch_vccnz .LBB0_1259
	v_cvt_f32_f16_sdwa v131, v174 dst_sel:DWORD dst_unused:UNUSED_PAD src0_sel:WORD_1
	v_cvt_f32_f16_e32 v130, v174
	s_waitcnt vmcnt(7)
	v_cvt_f32_f16_sdwa v133, v238 dst_sel:DWORD dst_unused:UNUSED_PAD src0_sel:WORD_1
	v_cvt_f32_f16_e32 v132, v238
	v_cvt_f32_f16_sdwa v135, v175 dst_sel:DWORD dst_unused:UNUSED_PAD src0_sel:WORD_1
	v_cvt_f32_f16_e32 v134, v175
	v_cvt_f32_f16_sdwa v137, v239 dst_sel:DWORD dst_unused:UNUSED_PAD src0_sel:WORD_1
	v_cvt_f32_f16_e32 v136, v239
	v_cvt_f32_f16_sdwa v139, v176 dst_sel:DWORD dst_unused:UNUSED_PAD src0_sel:WORD_1
	v_cvt_f32_f16_e32 v138, v176
	v_cvt_f32_f16_sdwa v141, v240 dst_sel:DWORD dst_unused:UNUSED_PAD src0_sel:WORD_1
	v_cvt_f32_f16_e32 v140, v240
	v_cvt_f32_f16_sdwa v143, v177 dst_sel:DWORD dst_unused:UNUSED_PAD src0_sel:WORD_1
	v_cvt_f32_f16_e32 v142, v177
	v_cvt_f32_f16_sdwa v145, v241 dst_sel:DWORD dst_unused:UNUSED_PAD src0_sel:WORD_1
	v_cvt_f32_f16_e32 v144, v241
	v_pk_add_f32 v[130:131], v[132:133], v[130:131]
	v_pk_add_f32 v[132:133], v[136:137], v[134:135]
	v_pk_add_f32 v[134:135], v[140:141], v[138:139]
	v_pk_add_f32 v[136:137], v[144:145], v[142:143]
	v_pk_add_f32 v[122:123], v[122:123], v[130:131]
	v_pk_add_f32 v[126:127], v[126:127], v[132:133]
	v_pk_add_f32 v[124:125], v[124:125], v[134:135]
	v_pk_add_f32 v[128:129], v[128:129], v[136:137]
.LBB0_1259:
	s_mov_b32 s26, 0x18000
	v_cvt_pk_f16_f32 v122, v122, v123
	v_cvt_pk_f16_f32 v123, v126, v127
	v_add_co_u32_e32 v126, vcc, s26, v178
	v_cvt_pk_f16_f32 v124, v124, v125
	v_cvt_pk_f16_f32 v125, v128, v129
	v_addc_co_u32_e32 v127, vcc, 0, v179, vcc
	global_store_dwordx4 v[126:127], v[122:125], off
	v_cvt_f32_i32_e32 v118, v118
	v_cvt_f32_i32_e32 v119, v119
	v_cvt_f32_i32_e32 v122, v120
	v_cvt_f32_i32_e32 v120, v114
	v_cvt_f32_i32_e32 v124, v115
	v_mul_f32_e32 v114, v38, v118
	v_fma_f32 v114, v221, v114, v34
	v_mul_f32_e32 v115, v30, v120
	v_fma_f32 v115, v221, v115, v26
	v_mul_f32_e32 v115, 0xbfb8aa3b, v115
	v_exp_f32_e32 v115, v115
	v_mul_f32_e32 v114, 0xbfb8aa3b, v114
	v_exp_f32_e32 v114, v114
	v_cvt_f32_i32_e32 v123, v121
	v_add_f32_e32 v115, 1.0, v115
	v_rcp_f32_e32 v118, v115
	v_mul_f32_e32 v115, v39, v119
	v_fma_f32 v115, v221, v115, v35
	v_mul_f32_e32 v115, 0xbfb8aa3b, v115
	v_exp_f32_e32 v115, v115
	v_mul_f32_e32 v119, v31, v124
	v_fma_f32 v119, v221, v119, v27
	v_mul_f32_e32 v119, 0xbfb8aa3b, v119
	v_add_f32_e32 v114, 1.0, v114
	v_add_f32_e32 v115, 1.0, v115
	v_exp_f32_e32 v119, v119
	v_rcp_f32_e32 v114, v114
	v_rcp_f32_e32 v115, v115
	s_cmp_lg_u64 s[36:37], 0
	s_cbranch_scc0 .Lg3w_31145
	s_waitcnt vmcnt(3)
	s_branch .Lg3j_31145

;     __device__ __forceinline__ void operator()(const f32x4 (&acc)[2][2][4][2], const Unit& u, int wr, int wc, int fr, int fq) const {
;     ...
;         for (int ai = 0; ai < 2; ++ai) {
;             const int rowa = row0 + ai * HALF; const size_t offa = (size_t)rowa * 1024 + (size_t)(rowa >> 12) * GAPY + col0;
; #pragma unroll
;             for (int mp = 0; mp < 2; ++mp) {
;             f16x8 yv[4][2];
; #pragma unroll
;             for (int m = 2 * mp; m < 2 * mp + 2; ++m)
; #pragma unroll
;                 for (int bj = 0; bj < 2; ++bj) yv[m][bj] = *(const g_f16x8*)(Yb + offa + (size_t)m * 16 * 1024 + bj * HALF);
; #pragma unroll
;             for (int m = 2 * mp; m < 2 * mp + 2; ++m) { const size_t off = offa + (size_t)m * 16 * 1024;
;                 f16x8 za[2], zb[2];
;                 if (br == 2) {
; #pragma unroll
;                     for (int bj = 0; bj < 2; ++bj) { za[bj] = *(const g_f16x8*)(Y + off + bj * HALF); zb[bj] = *(const g_f16x8*)(Y + YSTR + off + bj * HALF); } }
; #pragma unroll
;                 for (int bj = 0; bj < 2; ++bj) {
;                     f32x4 a0 = acc[ai][bj][m][0], a1 = acc[ai][bj][m][1];
;                     if constexpr (I8) { const i32x4 i0 = __builtin_bit_cast(i32x4, a0), i1 = __builtin_bit_cast(i32x4, a1);
;                         a0 = (f32x4){(float)i0.x, (float)i0.y, (float)i0.z, (float)i0.w} * sv[bj][0]; a1 = (f32x4){(float)i1.x, (float)i1.y, (float)i1.z, (float)i1.w} * sv[bj][1]; }
;                     const f32x4 g0 = a0 * rs[ai][m] + bv[bj][0], g1 = a1 * rs[ai][m] + bv[bj][1];
;                     const f16x8 yy = yv[m][bj];
;                     float z[8];
; #pragma unroll
;                     for (int e = 0; e < 4; ++e) { z[e] = (float)yy[e] * __builtin_amdgcn_rcpf(1.f + __builtin_amdgcn_exp2f(-LOG2E * g0[e])); z[4 + e] = (float)yy[4 + e] * __builtin_amdgcn_rcpf(1.f + __builtin_amdgcn_exp2f(-LOG2E * g1[e])); }
;                     if (br == 2) {
; #pragma unroll
;                         for (int e = 0; e < 8; ++e) z[e] += (float)za[bj][e] + (float)zb[bj][e]; }
;                     u32x4 w; w.x = pk2h(z[0], z[1]); w.y = pk2h(z[2], z[3]); w.z = pk2h(z[4], z[5]); w.w = pk2h(z[6], z[7]);
;                     f16* dst = (br == 2) ? merged : Yb;
;                     gst16(dst + off + bj * HALF, w); } } } }
.LBB0_1261:
	v_cvt_f32_i32_e32 v116, v116
	v_cvt_f32_i32_e32 v117, v117
	v_cvt_f32_f16_sdwa v123, v149 dst_sel:DWORD dst_unused:UNUSED_PAD src0_sel:WORD_1
	v_cvt_f32_f16_e32 v122, v149
	v_mul_f32_e32 v116, v32, v116
	v_mul_f32_e32 v117, v33, v117
	v_fma_f32 v116, v221, v116, v28
	v_fma_f32 v117, v221, v117, v29
	v_mul_f32_e32 v116, 0xbfb8aa3b, v116
	v_mul_f32_e32 v117, 0xbfb8aa3b, v117
	v_exp_f32_e32 v116, v116
	v_exp_f32_e32 v117, v117
	s_andn2_b64 vcc, exec, s[50:51]
	v_add_f32_e32 v116, 1.0, v116
	v_add_f32_e32 v117, 1.0, v117
	v_rcp_f32_e32 v116, v116
	v_rcp_f32_e32 v117, v117
	s_nop 0
	v_pk_mul_f32 v[116:117], v[116:117], v[122:123]
	s_cbranch_vccnz .LBB0_1263
	v_cvt_f32_f16_sdwa v123, v180 dst_sel:DWORD dst_unused:UNUSED_PAD src0_sel:WORD_1
	v_cvt_f32_f16_e32 v122, v180
	s_waitcnt vmcnt(7)
	v_cvt_f32_f16_sdwa v125, v246 dst_sel:DWORD dst_unused:UNUSED_PAD src0_sel:WORD_1
	v_cvt_f32_f16_e32 v124, v246
	v_cvt_f32_f16_sdwa v127, v181 dst_sel:DWORD dst_unused:UNUSED_PAD src0_sel:WORD_1
	v_cvt_f32_f16_e32 v126, v181
	v_cvt_f32_f16_sdwa v129, v247 dst_sel:DWORD dst_unused:UNUSED_PAD src0_sel:WORD_1
	v_cvt_f32_f16_e32 v128, v247
	v_cvt_f32_f16_sdwa v131, v182 dst_sel:DWORD dst_unused:UNUSED_PAD src0_sel:WORD_1
	v_cvt_f32_f16_e32 v130, v182
	v_cvt_f32_f16_sdwa v133, v248 dst_sel:DWORD dst_unused:UNUSED_PAD src0_sel:WORD_1
	v_cvt_f32_f16_e32 v132, v248
	v_cvt_f32_f16_sdwa v135, v183 dst_sel:DWORD dst_unused:UNUSED_PAD src0_sel:WORD_1
	v_cvt_f32_f16_e32 v134, v183
	v_cvt_f32_f16_sdwa v137, v249 dst_sel:DWORD dst_unused:UNUSED_PAD src0_sel:WORD_1
	v_cvt_f32_f16_e32 v136, v249
	v_pk_add_f32 v[122:123], v[124:125], v[122:123]
	v_pk_add_f32 v[124:125], v[128:129], v[126:127]
	v_pk_add_f32 v[126:127], v[132:133], v[130:131]
	v_pk_add_f32 v[128:129], v[136:137], v[134:135]
	v_pk_add_f32 v[114:115], v[114:115], v[122:123]
	v_pk_add_f32 v[120:121], v[120:121], v[124:125]
	v_pk_add_f32 v[118:119], v[118:119], v[126:127]
	v_pk_add_f32 v[116:117], v[116:117], v[128:129]
.LBB0_1263:
	v_cvt_pk_f16_f32 v122, v114, v115
	v_add_u32_e32 v114, 0x80, v218
	v_ashrrev_i32_e32 v115, 31, v114
	v_cvt_pk_f16_f32 v125, v116, v117
	v_lshlrev_b64 v[116:117], 10, v[114:115]
	v_cvt_pk_f16_f32 v124, v118, v119
	v_ashrrev_i32_e32 v118, 12, v114
	v_lshl_add_u64 v[114:115], v[116:117], 0, v[216:217]
	s_mov_b32 s26, 0xc00000
	v_mad_i64_i32 v[130:131], s[50:51], v118, s26, v[114:115]
	s_mov_b64 s[28:29], 0x18000
	v_lshl_add_u64 v[132:133], v[130:131], 1, s[48:49]
	v_lshl_add_u64 v[126:127], v[178:179], 0, s[28:29]
	v_cvt_pk_f16_f32 v123, v120, v121
	v_add_co_u32_e32 v114, vcc, 0x8000, v132
	global_store_dwordx4 v[126:127], v[122:125], off offset:256
	s_nop 0
	v_addc_co_u32_e32 v115, vcc, 0, v133, vcc
	global_load_dwordx4 v[126:129], v[132:133], off
	global_load_dwordx4 v[122:125], v[132:133], off offset:256
	global_load_dwordx4 v[118:121], v[114:115], off
	s_nop 0
	global_load_dwordx4 v[114:117], v[114:115], off offset:256
	s_and_b64 vcc, exec, s[36:37]
	s_cbranch_vccnz .LBB0_1265
	v_lshlrev_b64 v[42:43], 1, v[130:131]
	v_lshl_add_u64 v[44:45], s[40:41], 0, v[42:43]
	s_waitcnt vmcnt(14)
	v_lshl_add_u64 v[46:47], s[44:45], 0, v[42:43]
	s_nop 0
	s_nop 0
	s_nop 0
	s_mov_b64 s[28:29], 0x48000
	v_lshl_add_u64 v[150:151], v[228:229], 1, s[28:29]
	v_lshl_add_u64 v[220:221], s[44:45], 0, v[150:151]
	v_lshl_add_u64 v[150:151], s[40:41], 0, v[150:151]
	global_load_dwordx4 v[146:149], v[150:151], off
	global_load_dwordx4 v[150:153], v[150:151], off offset:256
	global_load_dwordx4 v[216:219], v[220:221], off
	global_load_dwordx4 v[220:223], v[220:221], off offset:256
	s_mov_b64 s[28:29], 0x50000
	v_lshl_add_u64 v[174:175], v[228:229], 1, s[28:29]
	v_lshl_add_u64 v[224:225], s[44:45], 0, v[174:175]
	v_lshl_add_u64 v[174:175], s[40:41], 0, v[174:175]
	global_load_dwordx4 v[170:173], v[174:175], off
	global_load_dwordx4 v[174:177], v[174:175], off offset:256
	global_load_dwordx4 v[178:181], v[224:225], off
	global_load_dwordx4 v[224:227], v[224:225], off offset:256
.LBB0_1265:
	v_cvt_f32_i32_e32 v134, v106
	v_cvt_f32_i32_e32 v135, v107
	v_cvt_f32_i32_e32 v110, v110
	v_cvt_f32_i32_e32 v111, v111
	v_mul_f32_e32 v107, v54, v134
	v_fma_f32 v107, v214, v107, v50
	v_mul_f32_e32 v107, 0xbfb8aa3b, v107
	v_exp_f32_e32 v107, v107
	v_cvt_f32_i32_e32 v136, v108
	v_mul_f32_e32 v106, v70, v110
	v_fma_f32 v106, v214, v106, v62
	v_add_f32_e32 v107, 1.0, v107
	v_rcp_f32_e32 v108, v107
	v_mul_f32_e32 v107, v71, v111
	v_fma_f32 v107, v214, v107, v63
	v_mul_f32_e32 v106, 0xbfb8aa3b, v106
	v_mul_f32_e32 v107, 0xbfb8aa3b, v107
	v_exp_f32_e32 v106, v106
	v_exp_f32_e32 v107, v107
	v_cvt_f32_i32_e32 v137, v109
	v_mul_f32_e32 v109, v55, v135
	v_fma_f32 v109, v214, v109, v51
	v_mul_f32_e32 v109, 0xbfb8aa3b, v109
	v_add_f32_e32 v106, 1.0, v106
	v_add_f32_e32 v107, 1.0, v107
	v_exp_f32_e32 v109, v109
	v_rcp_f32_e32 v106, v106
	v_rcp_f32_e32 v107, v107
	s_cmp_lg_u64 s[36:37], 0
	s_cbranch_scc0 .Lg3w_31289
	s_waitcnt vmcnt(3)
	s_branch .Lg3j_31289
.Lg3w_31289:
	s_waitcnt vmcnt(11)
; __device__ __forceinline__ unsigned pk2h(float lo, float hi) { f32x2 v = {lo, hi}; f16x2 h = __builtin_convertvector(v, f16x2); return __builtin_bit_cast(unsigned, h); }
;     __device__ __forceinline__ void operator()(const f32x4 (&acc)[2][2][4][2], const Unit& u, int wr, int wc, int fr, int fq) const {
;     ...
;             for (int m = 2 * mp; m < 2 * mp + 2; ++m) { const size_t off = offa + (size_t)m * 16 * 1024;
;                 f16x8 za[2], zb[2];
;                 if (br == 2) {
; #pragma unroll
;                     for (int bj = 0; bj < 2; ++bj) { za[bj] = *(const g_f16x8*)(Y + off + bj * HALF); zb[bj] = *(const g_f16x8*)(Y + YSTR + off + bj * HALF); } }
; #pragma unroll
;                 for (int bj = 0; bj < 2; ++bj) {
;                     f32x4 a0 = acc[ai][bj][m][0], a1 = acc[ai][bj][m][1];
;                     if constexpr (I8) { const i32x4 i0 = __builtin_bit_cast(i32x4, a0), i1 = __builtin_bit_cast(i32x4, a1);
;                         a0 = (f32x4){(float)i0.x, (float)i0.y, (float)i0.z, (float)i0.w} * sv[bj][0]; a1 = (f32x4){(float)i1.x, (float)i1.y, (float)i1.z, (float)i1.w} * sv[bj][1]; }
;                     const f32x4 g0 = a0 * rs[ai][m] + bv[bj][0], g1 = a1 * rs[ai][m] + bv[bj][1];
;                     const f16x8 yy = yv[m][bj];
;                     float z[8];
; #pragma unroll
;                     for (int e = 0; e < 4; ++e) { z[e] = (float)yy[e] * __builtin_amdgcn_rcpf(1.f + __builtin_amdgcn_exp2f(-LOG2E * g0[e])); z[4 + e] = (float)yy[4 + e] * __builtin_amdgcn_rcpf(1.f + __builtin_amdgcn_exp2f(-LOG2E * g1[e])); }
;                     if (br == 2) {
; #pragma unroll
;                         for (int e = 0; e < 8; ++e) z[e] += (float)za[bj][e] + (float)zb[bj][e]; }
;                     u32x4 w; w.x = pk2h(z[0], z[1]); w.y = pk2h(z[2], z[3]); w.z = pk2h(z[4], z[5]); w.w = pk2h(z[6], z[7]);
;                     f16* dst = (br == 2) ? merged : Yb;
;                     gst16(dst + off + bj * HALF, w); } } } }
.Lg3j_31289:
	v_cvt_f32_f16_sdwa v111, v126 dst_sel:DWORD dst_unused:UNUSED_PAD src0_sel:WORD_1
	v_cvt_f32_f16_e32 v110, v126
	v_add_f32_e32 v109, 1.0, v109
	v_rcp_f32_e32 v109, v109
	v_cvt_f32_i32_e32 v112, v112
	v_pk_mul_f32 v[106:107], v[106:107], v[110:111]
	v_cvt_f32_f16_sdwa v111, v128 dst_sel:DWORD dst_unused:UNUSED_PAD src0_sel:WORD_1
	v_cvt_f32_f16_e32 v110, v128
	v_cvt_f32_i32_e32 v113, v113
	v_cvt_f32_f16_sdwa v135, v127 dst_sel:DWORD dst_unused:UNUSED_PAD src0_sel:WORD_1
	v_cvt_f32_f16_e32 v134, v127
	v_pk_mul_f32 v[108:109], v[108:109], v[110:111]
	v_mul_f32_e32 v111, v56, v136
	v_fma_f32 v111, v214, v111, v52
	v_mul_f32_e32 v111, 0xbfb8aa3b, v111
	v_exp_f32_e32 v111, v111
	v_mul_f32_e32 v110, v72, v112
	v_fma_f32 v110, v214, v110, v64
	v_mul_f32_e32 v110, 0xbfb8aa3b, v110
	v_add_f32_e32 v111, 1.0, v111
	v_rcp_f32_e32 v112, v111
	v_mul_f32_e32 v111, v73, v113
	v_mul_f32_e32 v113, v57, v137
	v_fma_f32 v111, v214, v111, v65
	v_fma_f32 v113, v214, v113, v53
	v_mul_f32_e32 v111, 0xbfb8aa3b, v111
	v_mul_f32_e32 v113, 0xbfb8aa3b, v113
	v_exp_f32_e32 v110, v110
	v_exp_f32_e32 v111, v111
	v_exp_f32_e32 v113, v113
	v_cvt_f32_f16_sdwa v127, v129 dst_sel:DWORD dst_unused:UNUSED_PAD src0_sel:WORD_1
	v_add_f32_e32 v110, 1.0, v110
	v_add_f32_e32 v111, 1.0, v111
	v_add_f32_e32 v113, 1.0, v113
	v_rcp_f32_e32 v110, v110
	v_rcp_f32_e32 v111, v111
	v_rcp_f32_e32 v113, v113
	v_cvt_f32_f16_e32 v126, v129
	s_and_b64 vcc, exec, s[36:37]
	v_pk_mul_f32 v[110:111], v[110:111], v[134:135]
	v_pk_mul_f32 v[112:113], v[112:113], v[126:127]
	s_cbranch_vccnz .LBB0_1267
	v_cvt_f32_f16_sdwa v127, v154 dst_sel:DWORD dst_unused:UNUSED_PAD src0_sel:WORD_1
	v_cvt_f32_f16_e32 v126, v154
	s_waitcnt vmcnt(11)
	v_cvt_f32_f16_sdwa v129, v162 dst_sel:DWORD dst_unused:UNUSED_PAD src0_sel:WORD_1
	v_cvt_f32_f16_e32 v128, v162
	v_cvt_f32_f16_sdwa v135, v155 dst_sel:DWORD dst_unused:UNUSED_PAD src0_sel:WORD_1
	v_cvt_f32_f16_e32 v134, v155
	v_cvt_f32_f16_sdwa v137, v163 dst_sel:DWORD dst_unused:UNUSED_PAD src0_sel:WORD_1
	v_cvt_f32_f16_e32 v136, v163
	v_cvt_f32_f16_sdwa v139, v156 dst_sel:DWORD dst_unused:UNUSED_PAD src0_sel:WORD_1
	v_cvt_f32_f16_e32 v138, v156
	v_cvt_f32_f16_sdwa v141, v164 dst_sel:DWORD dst_unused:UNUSED_PAD src0_sel:WORD_1
	v_cvt_f32_f16_e32 v140, v164
	v_cvt_f32_f16_sdwa v143, v157 dst_sel:DWORD dst_unused:UNUSED_PAD src0_sel:WORD_1
	v_cvt_f32_f16_e32 v142, v157
	v_cvt_f32_f16_sdwa v145, v165 dst_sel:DWORD dst_unused:UNUSED_PAD src0_sel:WORD_1
	v_cvt_f32_f16_e32 v144, v165
	v_pk_add_f32 v[126:127], v[128:129], v[126:127]
	v_pk_add_f32 v[128:129], v[136:137], v[134:135]
	v_pk_add_f32 v[134:135], v[140:141], v[138:139]
	v_pk_add_f32 v[136:137], v[144:145], v[142:143]
	v_pk_add_f32 v[106:107], v[106:107], v[126:127]
	v_pk_add_f32 v[110:111], v[110:111], v[128:129]
	v_pk_add_f32 v[108:109], v[108:109], v[134:135]
	v_pk_add_f32 v[112:113], v[112:113], v[136:137]
.LBB0_1267:
	v_cvt_pk_f16_f32 v128, v108, v109
	v_cvt_f32_i32_e32 v108, v104
	v_cvt_f32_i32_e32 v104, v98
	v_cvt_pk_f16_f32 v127, v110, v111
	v_cvt_f32_i32_e32 v110, v99
	v_cvt_f32_i32_e32 v102, v102
	v_mul_f32_e32 v99, v30, v104
	v_fma_f32 v99, v214, v99, v26
	v_mul_f32_e32 v99, 0xbfb8aa3b, v99
	v_exp_f32_e32 v99, v99
	v_cvt_f32_i32_e32 v103, v103
	v_mul_f32_e32 v98, v38, v102
	v_fma_f32 v98, v214, v98, v34
	v_add_f32_e32 v99, 1.0, v99
	v_rcp_f32_e32 v102, v99
	v_mul_f32_e32 v99, v39, v103
	v_fma_f32 v99, v214, v99, v35
	v_mul_f32_e32 v98, 0xbfb8aa3b, v98
	v_mul_f32_e32 v99, 0xbfb8aa3b, v99
	v_exp_f32_e32 v98, v98
	v_exp_f32_e32 v99, v99
	v_mul_f32_e32 v103, v31, v110
	v_fma_f32 v103, v214, v103, v27
	v_mul_f32_e32 v103, 0xbfb8aa3b, v103
	v_add_f32_e32 v98, 1.0, v98
	v_add_f32_e32 v99, 1.0, v99
	v_exp_f32_e32 v103, v103
	v_cvt_f32_i32_e32 v109, v105
	v_rcp_f32_e32 v98, v98
	v_rcp_f32_e32 v99, v99
	s_cmp_lg_u64 s[36:37], 0
	s_cbranch_scc0 .Lg3w_31389
	s_waitcnt vmcnt(2)
	s_branch .Lg3j_31389
.Lg3w_31389:
	s_waitcnt vmcnt(10)
.Lg3j_31389:
	v_cvt_f32_f16_sdwa v105, v122 dst_sel:DWORD dst_unused:UNUSED_PAD src0_sel:WORD_1
	v_cvt_f32_f16_e32 v104, v122
	v_add_f32_e32 v103, 1.0, v103
	v_rcp_f32_e32 v103, v103
	v_cvt_pk_f16_f32 v126, v106, v107
	v_pk_mul_f32 v[98:99], v[98:99], v[104:105]
	v_cvt_f32_f16_sdwa v105, v124 dst_sel:DWORD dst_unused:UNUSED_PAD src0_sel:WORD_1
	v_cvt_f32_f16_e32 v104, v124
	v_cvt_pk_f16_f32 v129, v112, v113
	v_lshl_add_u64 v[106:107], v[130:131], 1, s[46:47]
	s_mov_b64 s[46:47], -1
	v_pk_mul_f32 v[102:103], v[102:103], v[104:105]
	v_mul_f32_e32 v104, v40, v108
	v_mul_f32_e32 v105, v41, v109
	v_fma_f32 v104, v214, v104, v36
	v_fma_f32 v105, v214, v105, v37
	v_mul_f32_e32 v104, 0xbfb8aa3b, v104
	v_mul_f32_e32 v105, 0xbfb8aa3b, v105
	v_exp_f32_e32 v104, v104
	v_exp_f32_e32 v105, v105
	v_cvt_f32_f16_sdwa v109, v123 dst_sel:DWORD dst_unused:UNUSED_PAD src0_sel:WORD_1
	v_cvt_f32_f16_e32 v108, v123
	v_add_f32_e32 v104, 1.0, v104
	v_add_f32_e32 v105, 1.0, v105
	v_rcp_f32_e32 v104, v104
	v_rcp_f32_e32 v105, v105
	s_and_b64 vcc, exec, s[38:39]
	global_store_dwordx4 v[106:107], v[126:129], off
	v_pk_mul_f32 v[104:105], v[104:105], v[108:109]
	s_cbranch_vccnz .LBB0_1269
	s_mov_b64 s[46:47], 0
; __device__ __forceinline__ unsigned pk2h(float lo, float hi) { f32x2 v = {lo, hi}; f16x2 h = __builtin_convertvector(v, f16x2); return __builtin_bit_cast(unsigned, h); }
;     __device__ __forceinline__ void operator()(const f32x4 (&acc)[2][2][4][2], const Unit& u, int wr, int wc, int fr, int fq) const {
;     ...
;             for (int m = 2 * mp; m < 2 * mp + 2; ++m) { const size_t off = offa + (size_t)m * 16 * 1024;
;                 f16x8 za[2], zb[2];
;                 if (br == 2) {
; #pragma unroll
;                     for (int bj = 0; bj < 2; ++bj) { za[bj] = *(const g_f16x8*)(Y + off + bj * HALF); zb[bj] = *(const g_f16x8*)(Y + YSTR + off + bj * HALF); } }
; #pragma unroll
;                 for (int bj = 0; bj < 2; ++bj) {
;                     f32x4 a0 = acc[ai][bj][m][0], a1 = acc[ai][bj][m][1];
;                     if constexpr (I8) { const i32x4 i0 = __builtin_bit_cast(i32x4, a0), i1 = __builtin_bit_cast(i32x4, a1);
;                         a0 = (f32x4){(float)i0.x, (float)i0.y, (float)i0.z, (float)i0.w} * sv[bj][0]; a1 = (f32x4){(float)i1.x, (float)i1.y, (float)i1.z, (float)i1.w} * sv[bj][1]; }
;                     const f32x4 g0 = a0 * rs[ai][m] + bv[bj][0], g1 = a1 * rs[ai][m] + bv[bj][1];
;                     const f16x8 yy = yv[m][bj];
;                     float z[8];
; #pragma unroll
;                     for (int e = 0; e < 4; ++e) { z[e] = (float)yy[e] * __builtin_amdgcn_rcpf(1.f + __builtin_amdgcn_exp2f(-LOG2E * g0[e])); z[4 + e] = (float)yy[4 + e] * __builtin_amdgcn_rcpf(1.f + __builtin_amdgcn_exp2f(-LOG2E * g1[e])); }
;                     if (br == 2) {
; #pragma unroll
;                         for (int e = 0; e < 8; ++e) z[e] += (float)za[bj][e] + (float)zb[bj][e]; }
;                     u32x4 w; w.x = pk2h(z[0], z[1]); w.y = pk2h(z[2], z[3]); w.z = pk2h(z[4], z[5]); w.w = pk2h(z[6], z[7]);
;                     f16* dst = (br == 2) ? merged : Yb;
;                     gst16(dst + off + bj * HALF, w); } } } }
.LBB0_1269:
	v_cvt_f32_i32_e32 v100, v100
	v_cvt_f32_i32_e32 v101, v101
	v_cvt_f32_f16_sdwa v109, v125 dst_sel:DWORD dst_unused:UNUSED_PAD src0_sel:WORD_1
	v_cvt_f32_f16_e32 v108, v125
	v_mul_f32_e32 v100, v32, v100
	v_mul_f32_e32 v101, v33, v101
	v_fma_f32 v100, v214, v100, v28
	v_fma_f32 v101, v214, v101, v29
	v_mul_f32_e32 v100, 0xbfb8aa3b, v100
	v_mul_f32_e32 v101, 0xbfb8aa3b, v101
	v_exp_f32_e32 v100, v100
	v_exp_f32_e32 v101, v101
	s_andn2_b64 vcc, exec, s[46:47]
	v_add_f32_e32 v100, 1.0, v100
	v_add_f32_e32 v101, 1.0, v101
	v_rcp_f32_e32 v100, v100
	v_rcp_f32_e32 v101, v101
	s_nop 0
	v_pk_mul_f32 v[100:101], v[100:101], v[108:109]
	s_cbranch_vccnz .LBB0_1271
	v_cvt_f32_f16_sdwa v109, v158 dst_sel:DWORD dst_unused:UNUSED_PAD src0_sel:WORD_1
	v_cvt_f32_f16_e32 v108, v158
	s_waitcnt vmcnt(11)
	v_cvt_f32_f16_sdwa v111, v166 dst_sel:DWORD dst_unused:UNUSED_PAD src0_sel:WORD_1
	v_cvt_f32_f16_e32 v110, v166
	v_cvt_f32_f16_sdwa v113, v159 dst_sel:DWORD dst_unused:UNUSED_PAD src0_sel:WORD_1
	v_cvt_f32_f16_e32 v112, v159
	v_cvt_f32_f16_sdwa v123, v167 dst_sel:DWORD dst_unused:UNUSED_PAD src0_sel:WORD_1
	v_cvt_f32_f16_e32 v122, v167
	v_cvt_f32_f16_sdwa v125, v160 dst_sel:DWORD dst_unused:UNUSED_PAD src0_sel:WORD_1
	v_cvt_f32_f16_e32 v124, v160
	v_cvt_f32_f16_sdwa v127, v168 dst_sel:DWORD dst_unused:UNUSED_PAD src0_sel:WORD_1
	v_cvt_f32_f16_e32 v126, v168
	v_cvt_f32_f16_sdwa v129, v161 dst_sel:DWORD dst_unused:UNUSED_PAD src0_sel:WORD_1
	v_cvt_f32_f16_e32 v128, v161
	v_cvt_f32_f16_sdwa v135, v169 dst_sel:DWORD dst_unused:UNUSED_PAD src0_sel:WORD_1
	v_cvt_f32_f16_e32 v134, v169
	v_pk_add_f32 v[108:109], v[110:111], v[108:109]
	v_pk_add_f32 v[110:111], v[122:123], v[112:113]
	v_pk_add_f32 v[112:113], v[126:127], v[124:125]
	v_pk_add_f32 v[122:123], v[134:135], v[128:129]
	v_pk_add_f32 v[98:99], v[98:99], v[108:109]
	v_pk_add_f32 v[104:105], v[104:105], v[110:111]
	v_pk_add_f32 v[102:103], v[102:103], v[112:113]
	v_pk_add_f32 v[100:101], v[100:101], v[122:123]
.LBB0_1271:
	v_cvt_pk_f16_f32 v108, v98, v99
	v_cvt_pk_f16_f32 v109, v104, v105
	v_cvt_pk_f16_f32 v110, v102, v103
	v_cvt_pk_f16_f32 v111, v100, v101
	s_and_b64 vcc, exec, s[36:37]
	global_store_dwordx4 v[106:107], v[108:111], off offset:256
	s_cbranch_vccnz .LBB0_1273
	v_mov_b64_e32 v[42:43], 0x8000
	v_lshl_add_u64 v[42:43], v[130:131], 1, v[42:43]
	v_lshl_add_u64 v[44:45], s[40:41], 0, v[42:43]
	s_waitcnt vmcnt(16)
	v_lshl_add_u64 v[46:47], s[44:45], 0, v[42:43]
	s_nop 0
	s_nop 0
	s_nop 0
	s_mov_b64 s[28:29], 0x58000
	v_lshl_add_u64 v[158:159], v[228:229], 1, s[28:29]
	v_lshl_add_u64 v[166:167], s[44:45], 0, v[158:159]
	v_lshl_add_u64 v[158:159], s[40:41], 0, v[158:159]
	global_load_dwordx4 v[154:157], v[158:159], off
	global_load_dwordx4 v[158:161], v[158:159], off offset:256
	global_load_dwordx4 v[162:165], v[166:167], off
	global_load_dwordx4 v[166:169], v[166:167], off offset:256
.LBB0_1273:
	v_cvt_f32_i32_e32 v98, v90
	v_cvt_f32_i32_e32 v99, v91
	v_cvt_f32_i32_e32 v94, v94
	v_cvt_f32_i32_e32 v95, v95
	v_mul_f32_e32 v91, v54, v98
	v_fma_f32 v91, v215, v91, v50
	v_mul_f32_e32 v91, 0xbfb8aa3b, v91
	v_exp_f32_e32 v91, v91
	v_cvt_f32_i32_e32 v100, v92
	v_mul_f32_e32 v90, v70, v94
	v_fma_f32 v90, v215, v90, v62
	v_add_f32_e32 v91, 1.0, v91
	v_rcp_f32_e32 v92, v91
	v_mul_f32_e32 v91, v71, v95
	v_fma_f32 v91, v215, v91, v63
	v_mul_f32_e32 v90, 0xbfb8aa3b, v90
	v_mul_f32_e32 v91, 0xbfb8aa3b, v91
	v_exp_f32_e32 v90, v90
	v_exp_f32_e32 v91, v91
	v_cvt_f32_i32_e32 v101, v93
	v_mul_f32_e32 v93, v55, v99
	v_fma_f32 v93, v215, v93, v51
	v_mul_f32_e32 v93, 0xbfb8aa3b, v93
	v_add_f32_e32 v90, 1.0, v90
	v_add_f32_e32 v91, 1.0, v91
	v_exp_f32_e32 v93, v93
	v_rcp_f32_e32 v90, v90
	v_rcp_f32_e32 v91, v91
	s_cmp_lg_u64 s[36:37], 0
	s_cbranch_scc0 .Lg3w_31519
	s_waitcnt vmcnt(3)
	s_branch .Lg3j_31519
.Lg3w_31519:
	s_waitcnt vmcnt(13)
; __device__ __forceinline__ unsigned pk2h(float lo, float hi) { f32x2 v = {lo, hi}; f16x2 h = __builtin_convertvector(v, f16x2); return __builtin_bit_cast(unsigned, h); }
;     __device__ __forceinline__ void operator()(const f32x4 (&acc)[2][2][4][2], const Unit& u, int wr, int wc, int fr, int fq) const {
;     ...
;             for (int m = 2 * mp; m < 2 * mp + 2; ++m) { const size_t off = offa + (size_t)m * 16 * 1024;
;                 f16x8 za[2], zb[2];
;                 if (br == 2) {
; #pragma unroll
;                     for (int bj = 0; bj < 2; ++bj) { za[bj] = *(const g_f16x8*)(Y + off + bj * HALF); zb[bj] = *(const g_f16x8*)(Y + YSTR + off + bj * HALF); } }
; #pragma unroll
;                 for (int bj = 0; bj < 2; ++bj) {
;                     f32x4 a0 = acc[ai][bj][m][0], a1 = acc[ai][bj][m][1];
;                     if constexpr (I8) { const i32x4 i0 = __builtin_bit_cast(i32x4, a0), i1 = __builtin_bit_cast(i32x4, a1);
;                         a0 = (f32x4){(float)i0.x, (float)i0.y, (float)i0.z, (float)i0.w} * sv[bj][0]; a1 = (f32x4){(float)i1.x, (float)i1.y, (float)i1.z, (float)i1.w} * sv[bj][1]; }
;                     const f32x4 g0 = a0 * rs[ai][m] + bv[bj][0], g1 = a1 * rs[ai][m] + bv[bj][1];
;                     const f16x8 yy = yv[m][bj];
;                     float z[8];
; #pragma unroll
;                     for (int e = 0; e < 4; ++e) { z[e] = (float)yy[e] * __builtin_amdgcn_rcpf(1.f + __builtin_amdgcn_exp2f(-LOG2E * g0[e])); z[4 + e] = (float)yy[4 + e] * __builtin_amdgcn_rcpf(1.f + __builtin_amdgcn_exp2f(-LOG2E * g1[e])); }
;                     if (br == 2) {
; #pragma unroll
;                         for (int e = 0; e < 8; ++e) z[e] += (float)za[bj][e] + (float)zb[bj][e]; }
;                     u32x4 w; w.x = pk2h(z[0], z[1]); w.y = pk2h(z[2], z[3]); w.z = pk2h(z[4], z[5]); w.w = pk2h(z[6], z[7]);
;                     f16* dst = (br == 2) ? merged : Yb;
;                     gst16(dst + off + bj * HALF, w); } } } }
.Lg3j_31519:
	v_cvt_f32_f16_sdwa v95, v118 dst_sel:DWORD dst_unused:UNUSED_PAD src0_sel:WORD_1
	v_cvt_f32_f16_e32 v94, v118
	v_add_f32_e32 v93, 1.0, v93
	v_rcp_f32_e32 v93, v93
	v_cvt_f32_i32_e32 v96, v96
	v_pk_mul_f32 v[90:91], v[90:91], v[94:95]
	v_cvt_f32_f16_sdwa v95, v120 dst_sel:DWORD dst_unused:UNUSED_PAD src0_sel:WORD_1
	v_cvt_f32_f16_e32 v94, v120
	v_cvt_f32_i32_e32 v97, v97
	v_cvt_f32_f16_sdwa v99, v119 dst_sel:DWORD dst_unused:UNUSED_PAD src0_sel:WORD_1
	v_cvt_f32_f16_e32 v98, v119
	v_pk_mul_f32 v[92:93], v[92:93], v[94:95]
	v_mul_f32_e32 v95, v56, v100
	v_fma_f32 v95, v215, v95, v52
	v_mul_f32_e32 v95, 0xbfb8aa3b, v95
	v_exp_f32_e32 v95, v95
	v_mul_f32_e32 v94, v72, v96
	v_fma_f32 v94, v215, v94, v64
	v_mul_f32_e32 v94, 0xbfb8aa3b, v94
	v_add_f32_e32 v95, 1.0, v95
	v_rcp_f32_e32 v96, v95
	v_mul_f32_e32 v95, v73, v97
	v_fma_f32 v95, v215, v95, v65
	v_mul_f32_e32 v95, 0xbfb8aa3b, v95
	v_exp_f32_e32 v94, v94
	v_exp_f32_e32 v95, v95
	v_mul_f32_e32 v97, v57, v101
	v_fma_f32 v97, v215, v97, v53
	v_mul_f32_e32 v97, 0xbfb8aa3b, v97
	v_add_f32_e32 v94, 1.0, v94
	v_add_f32_e32 v95, 1.0, v95
	v_exp_f32_e32 v97, v97
	v_rcp_f32_e32 v94, v94
	v_rcp_f32_e32 v95, v95
	s_and_b64 vcc, exec, s[36:37]
	v_add_f32_e32 v97, 1.0, v97
	v_rcp_f32_e32 v97, v97
	v_pk_mul_f32 v[94:95], v[94:95], v[98:99]
	v_cvt_f32_f16_sdwa v99, v121 dst_sel:DWORD dst_unused:UNUSED_PAD src0_sel:WORD_1
	v_cvt_f32_f16_e32 v98, v121
	v_pk_mul_f32 v[96:97], v[96:97], v[98:99]
	s_cbranch_vccnz .LBB0_1275
	v_cvt_f32_f16_sdwa v99, v146 dst_sel:DWORD dst_unused:UNUSED_PAD src0_sel:WORD_1
	v_cvt_f32_f16_e32 v98, v146
	s_waitcnt vmcnt(11)
	v_cvt_f32_f16_sdwa v101, v216 dst_sel:DWORD dst_unused:UNUSED_PAD src0_sel:WORD_1
	v_cvt_f32_f16_e32 v100, v216
	v_cvt_f32_f16_sdwa v103, v147 dst_sel:DWORD dst_unused:UNUSED_PAD src0_sel:WORD_1
	v_cvt_f32_f16_e32 v102, v147
	v_cvt_f32_f16_sdwa v105, v217 dst_sel:DWORD dst_unused:UNUSED_PAD src0_sel:WORD_1
	v_cvt_f32_f16_e32 v104, v217
	v_cvt_f32_f16_sdwa v109, v148 dst_sel:DWORD dst_unused:UNUSED_PAD src0_sel:WORD_1
	v_cvt_f32_f16_e32 v108, v148
	v_cvt_f32_f16_sdwa v111, v218 dst_sel:DWORD dst_unused:UNUSED_PAD src0_sel:WORD_1
	v_cvt_f32_f16_e32 v110, v218
	v_cvt_f32_f16_sdwa v113, v149 dst_sel:DWORD dst_unused:UNUSED_PAD src0_sel:WORD_1
	v_cvt_f32_f16_e32 v112, v149
	v_cvt_f32_f16_sdwa v119, v219 dst_sel:DWORD dst_unused:UNUSED_PAD src0_sel:WORD_1
	v_cvt_f32_f16_e32 v118, v219
	v_pk_add_f32 v[98:99], v[100:101], v[98:99]
	v_pk_add_f32 v[100:101], v[104:105], v[102:103]
	v_pk_add_f32 v[102:103], v[110:111], v[108:109]
	v_pk_add_f32 v[104:105], v[118:119], v[112:113]
	v_pk_add_f32 v[90:91], v[90:91], v[98:99]
	v_pk_add_f32 v[94:95], v[94:95], v[100:101]
	v_pk_add_f32 v[92:93], v[92:93], v[102:103]
	v_pk_add_f32 v[96:97], v[96:97], v[104:105]
.LBB0_1275:
	s_mov_b32 s26, 0x8000
	v_cvt_pk_f16_f32 v90, v90, v91
	v_cvt_pk_f16_f32 v91, v94, v95
	v_add_co_u32_e32 v94, vcc, s26, v106
	v_cvt_pk_f16_f32 v92, v92, v93
	v_cvt_pk_f16_f32 v93, v96, v97
	v_addc_co_u32_e32 v95, vcc, 0, v107, vcc
	global_store_dwordx4 v[94:95], v[90:93], off
	v_cvt_f32_i32_e32 v86, v86
	v_cvt_f32_i32_e32 v87, v87
	v_cvt_f32_i32_e32 v90, v88
	v_cvt_f32_i32_e32 v88, v82
	v_cvt_f32_i32_e32 v92, v83
	v_mul_f32_e32 v82, v38, v86
	v_fma_f32 v82, v215, v82, v34
	v_mul_f32_e32 v83, v30, v88
	v_fma_f32 v83, v215, v83, v26
	v_mul_f32_e32 v83, 0xbfb8aa3b, v83
	v_exp_f32_e32 v83, v83
	v_mul_f32_e32 v82, 0xbfb8aa3b, v82
	v_exp_f32_e32 v82, v82
	v_cvt_f32_i32_e32 v91, v89
	v_add_f32_e32 v83, 1.0, v83
	v_rcp_f32_e32 v86, v83
	v_mul_f32_e32 v83, v39, v87
	v_fma_f32 v83, v215, v83, v35
	v_mul_f32_e32 v83, 0xbfb8aa3b, v83
	v_exp_f32_e32 v83, v83
	v_mul_f32_e32 v87, v31, v92
	v_fma_f32 v87, v215, v87, v27
	v_mul_f32_e32 v87, 0xbfb8aa3b, v87
	v_add_f32_e32 v82, 1.0, v82
	v_add_f32_e32 v83, 1.0, v83
	v_exp_f32_e32 v87, v87
	v_rcp_f32_e32 v82, v82
	v_rcp_f32_e32 v83, v83
	s_cmp_lg_u64 s[36:37], 0
	s_cbranch_scc0 .Lg3w_31625
	s_waitcnt vmcnt(3)
	s_branch .Lg3j_31625

; __device__ __forceinline__ unsigned pk2h(float lo, float hi) { f32x2 v = {lo, hi}; f16x2 h = __builtin_convertvector(v, f16x2); return __builtin_bit_cast(unsigned, h); }
;     __device__ __forceinline__ void operator()(const f32x4 (&acc)[2][2][4][2], const Unit& u, int wr, int wc, int fr, int fq) const {
;     ...
;             for (int mp = 0; mp < 2; ++mp) {
;             f16x8 yv[4][2];
; #pragma unroll
;             for (int m = 2 * mp; m < 2 * mp + 2; ++m)
; #pragma unroll
;                 for (int bj = 0; bj < 2; ++bj) yv[m][bj] = *(const g_f16x8*)(Yb + offa + (size_t)m * 16 * 1024 + bj * HALF);
; #pragma unroll
;             for (int m = 2 * mp; m < 2 * mp + 2; ++m) { const size_t off = offa + (size_t)m * 16 * 1024;
;                 f16x8 za[2], zb[2];
;                 if (br == 2) {
; #pragma unroll
;                     for (int bj = 0; bj < 2; ++bj) { za[bj] = *(const g_f16x8*)(Y + off + bj * HALF); zb[bj] = *(const g_f16x8*)(Y + YSTR + off + bj * HALF); } }
; #pragma unroll
;                 for (int bj = 0; bj < 2; ++bj) {
;                     f32x4 a0 = acc[ai][bj][m][0], a1 = acc[ai][bj][m][1];
;                     if constexpr (I8) { const i32x4 i0 = __builtin_bit_cast(i32x4, a0), i1 = __builtin_bit_cast(i32x4, a1);
;                         a0 = (f32x4){(float)i0.x, (float)i0.y, (float)i0.z, (float)i0.w} * sv[bj][0]; a1 = (f32x4){(float)i1.x, (float)i1.y, (float)i1.z, (float)i1.w} * sv[bj][1]; }
;                     const f32x4 g0 = a0 * rs[ai][m] + bv[bj][0], g1 = a1 * rs[ai][m] + bv[bj][1];
;                     const f16x8 yy = yv[m][bj];
;                     float z[8];
; #pragma unroll
;                     for (int e = 0; e < 4; ++e) { z[e] = (float)yy[e] * __builtin_amdgcn_rcpf(1.f + __builtin_amdgcn_exp2f(-LOG2E * g0[e])); z[4 + e] = (float)yy[4 + e] * __builtin_amdgcn_rcpf(1.f + __builtin_amdgcn_exp2f(-LOG2E * g1[e])); }
;                     if (br == 2) {
; #pragma unroll
;                         for (int e = 0; e < 8; ++e) z[e] += (float)za[bj][e] + (float)zb[bj][e]; }
;                     u32x4 w; w.x = pk2h(z[0], z[1]); w.y = pk2h(z[2], z[3]); w.z = pk2h(z[4], z[5]); w.w = pk2h(z[6], z[7]);
;                     f16* dst = (br == 2) ? merged : Yb;
;                     gst16(dst + off + bj * HALF, w); } } } }
.Lg3j_31625:
	v_cvt_f32_f16_sdwa v89, v114 dst_sel:DWORD dst_unused:UNUSED_PAD src0_sel:WORD_1
	v_cvt_f32_f16_e32 v88, v114
	v_add_f32_e32 v87, 1.0, v87
	v_rcp_f32_e32 v87, v87
	s_mov_b64 s[46:47], -1
	v_pk_mul_f32 v[82:83], v[82:83], v[88:89]
	v_cvt_f32_f16_sdwa v89, v116 dst_sel:DWORD dst_unused:UNUSED_PAD src0_sel:WORD_1
	v_cvt_f32_f16_e32 v88, v116
	s_and_b64 vcc, exec, s[38:39]
	v_pk_mul_f32 v[86:87], v[86:87], v[88:89]
	v_mul_f32_e32 v88, v40, v90
	v_mul_f32_e32 v89, v41, v91
	v_fma_f32 v88, v215, v88, v36
	v_fma_f32 v89, v215, v89, v37
	v_mul_f32_e32 v88, 0xbfb8aa3b, v88
	v_mul_f32_e32 v89, 0xbfb8aa3b, v89
	v_exp_f32_e32 v88, v88
	v_exp_f32_e32 v89, v89
	v_cvt_f32_f16_sdwa v91, v115 dst_sel:DWORD dst_unused:UNUSED_PAD src0_sel:WORD_1
	v_cvt_f32_f16_e32 v90, v115
	v_add_f32_e32 v88, 1.0, v88
	v_add_f32_e32 v89, 1.0, v89
	v_rcp_f32_e32 v88, v88
	v_rcp_f32_e32 v89, v89
	s_nop 0
	v_pk_mul_f32 v[88:89], v[88:89], v[90:91]
	s_cbranch_vccnz .LBB0_1277
	s_mov_b64 s[46:47], 0
.LBB0_1277:
	v_cvt_f32_i32_e32 v84, v84
	v_cvt_f32_i32_e32 v85, v85
	v_cvt_f32_f16_sdwa v91, v117 dst_sel:DWORD dst_unused:UNUSED_PAD src0_sel:WORD_1
	v_cvt_f32_f16_e32 v90, v117
	v_mul_f32_e32 v84, v32, v84
	v_mul_f32_e32 v85, v33, v85
	v_fma_f32 v84, v215, v84, v28
	v_fma_f32 v85, v215, v85, v29
	v_mul_f32_e32 v84, 0xbfb8aa3b, v84
	v_mul_f32_e32 v85, 0xbfb8aa3b, v85
	v_exp_f32_e32 v84, v84
	v_exp_f32_e32 v85, v85
	s_andn2_b64 vcc, exec, s[46:47]
	v_add_f32_e32 v84, 1.0, v84
	v_add_f32_e32 v85, 1.0, v85
	v_rcp_f32_e32 v84, v84
	v_rcp_f32_e32 v85, v85
	s_nop 0
	v_pk_mul_f32 v[84:85], v[84:85], v[90:91]
	s_cbranch_vccnz .LBB0_1279
	v_cvt_f32_f16_sdwa v91, v150 dst_sel:DWORD dst_unused:UNUSED_PAD src0_sel:WORD_1
	v_cvt_f32_f16_e32 v90, v150
	s_waitcnt vmcnt(11)
	v_cvt_f32_f16_sdwa v93, v220 dst_sel:DWORD dst_unused:UNUSED_PAD src0_sel:WORD_1
	v_cvt_f32_f16_e32 v92, v220
	v_cvt_f32_f16_sdwa v95, v151 dst_sel:DWORD dst_unused:UNUSED_PAD src0_sel:WORD_1
	v_cvt_f32_f16_e32 v94, v151
	v_cvt_f32_f16_sdwa v97, v221 dst_sel:DWORD dst_unused:UNUSED_PAD src0_sel:WORD_1
	v_cvt_f32_f16_e32 v96, v221
	v_cvt_f32_f16_sdwa v99, v152 dst_sel:DWORD dst_unused:UNUSED_PAD src0_sel:WORD_1
	v_cvt_f32_f16_e32 v98, v152
	v_cvt_f32_f16_sdwa v101, v222 dst_sel:DWORD dst_unused:UNUSED_PAD src0_sel:WORD_1
	v_cvt_f32_f16_e32 v100, v222
	v_cvt_f32_f16_sdwa v103, v153 dst_sel:DWORD dst_unused:UNUSED_PAD src0_sel:WORD_1
	v_cvt_f32_f16_e32 v102, v153
	v_cvt_f32_f16_sdwa v105, v223 dst_sel:DWORD dst_unused:UNUSED_PAD src0_sel:WORD_1
	v_cvt_f32_f16_e32 v104, v223
	v_pk_add_f32 v[90:91], v[92:93], v[90:91]
	v_pk_add_f32 v[92:93], v[96:97], v[94:95]
	v_pk_add_f32 v[94:95], v[100:101], v[98:99]
	v_pk_add_f32 v[96:97], v[104:105], v[102:103]
	v_pk_add_f32 v[82:83], v[82:83], v[90:91]
	v_pk_add_f32 v[88:89], v[88:89], v[92:93]
	v_pk_add_f32 v[86:87], v[86:87], v[94:95]
	v_pk_add_f32 v[84:85], v[84:85], v[96:97]
.LBB0_1279:
	s_mov_b64 s[28:29], 0x8000
	v_lshl_add_u64 v[94:95], v[106:107], 0, s[28:29]
	v_cvt_pk_f16_f32 v90, v82, v83
	v_cvt_pk_f16_f32 v91, v88, v89
	v_cvt_pk_f16_f32 v92, v86, v87
	v_cvt_pk_f16_f32 v93, v84, v85
	v_add_co_u32_e32 v82, vcc, 0x10000, v132
	global_store_dwordx4 v[94:95], v[90:93], off offset:256
	s_nop 0
	v_addc_co_u32_e32 v83, vcc, 0, v133, vcc
	global_load_dwordx4 v[94:97], v[82:83], off
	global_load_dwordx4 v[90:93], v[82:83], off offset:256
	v_add_co_u32_e32 v82, vcc, 0x18000, v132
	s_nop 1
	v_addc_co_u32_e32 v83, vcc, 0, v133, vcc
	global_load_dwordx4 v[86:89], v[82:83], off
	s_nop 0
	global_load_dwordx4 v[82:85], v[82:83], off offset:256
	s_and_b64 vcc, exec, s[36:37]
	s_cbranch_vccnz .LBB0_1281
	v_mov_b64_e32 v[42:43], 0x10000
	v_lshl_add_u64 v[42:43], v[130:131], 1, v[42:43]
	v_lshl_add_u64 v[44:45], s[40:41], 0, v[42:43]
	s_waitcnt vmcnt(36)
	v_lshl_add_u64 v[46:47], s[44:45], 0, v[42:43]
	s_nop 0
	s_nop 0
	s_nop 0
; __device__ __forceinline__ unsigned pk2h(float lo, float hi) { f32x2 v = {lo, hi}; f16x2 h = __builtin_convertvector(v, f16x2); return __builtin_bit_cast(unsigned, h); }
;     __device__ __forceinline__ void operator()(const f32x4 (&acc)[2][2][4][2], const Unit& u, int wr, int wc, int fr, int fq) const {
;     ...
;             for (int m = 2 * mp; m < 2 * mp + 2; ++m) { const size_t off = offa + (size_t)m * 16 * 1024;
;                 f16x8 za[2], zb[2];
;                 if (br == 2) {
; #pragma unroll
;                     for (int bj = 0; bj < 2; ++bj) { za[bj] = *(const g_f16x8*)(Y + off + bj * HALF); zb[bj] = *(const g_f16x8*)(Y + YSTR + off + bj * HALF); } }
; #pragma unroll
;                 for (int bj = 0; bj < 2; ++bj) {
;                     f32x4 a0 = acc[ai][bj][m][0], a1 = acc[ai][bj][m][1];
;                     if constexpr (I8) { const i32x4 i0 = __builtin_bit_cast(i32x4, a0), i1 = __builtin_bit_cast(i32x4, a1);
;                         a0 = (f32x4){(float)i0.x, (float)i0.y, (float)i0.z, (float)i0.w} * sv[bj][0]; a1 = (f32x4){(float)i1.x, (float)i1.y, (float)i1.z, (float)i1.w} * sv[bj][1]; }
;                     const f32x4 g0 = a0 * rs[ai][m] + bv[bj][0], g1 = a1 * rs[ai][m] + bv[bj][1];
;                     const f16x8 yy = yv[m][bj];
;                     float z[8];
; #pragma unroll
;                     for (int e = 0; e < 4; ++e) { z[e] = (float)yy[e] * __builtin_amdgcn_rcpf(1.f + __builtin_amdgcn_exp2f(-LOG2E * g0[e])); z[4 + e] = (float)yy[4 + e] * __builtin_amdgcn_rcpf(1.f + __builtin_amdgcn_exp2f(-LOG2E * g1[e])); }
;                     if (br == 2) {
; #pragma unroll
;                         for (int e = 0; e < 8; ++e) z[e] += (float)za[bj][e] + (float)zb[bj][e]; }
;                     u32x4 w; w.x = pk2h(z[0], z[1]); w.y = pk2h(z[2], z[3]); w.z = pk2h(z[4], z[5]); w.w = pk2h(z[6], z[7]);
;                     f16* dst = (br == 2) ? merged : Yb;
;                     gst16(dst + off + bj * HALF, w); } } } }
.LBB0_1281:
	v_cvt_f32_i32_e32 v98, v74
	v_cvt_f32_i32_e32 v99, v75
	v_cvt_f32_i32_e32 v78, v78
	v_cvt_f32_i32_e32 v79, v79
	v_mul_f32_e32 v75, v54, v98
	v_fma_f32 v75, v212, v75, v50
	v_mul_f32_e32 v75, 0xbfb8aa3b, v75
	v_exp_f32_e32 v75, v75
	v_cvt_f32_i32_e32 v100, v76
	v_mul_f32_e32 v74, v70, v78
	v_fma_f32 v74, v212, v74, v62
	v_add_f32_e32 v75, 1.0, v75
	v_rcp_f32_e32 v76, v75
	v_mul_f32_e32 v75, v71, v79
	v_fma_f32 v75, v212, v75, v63
	v_mul_f32_e32 v74, 0xbfb8aa3b, v74
	v_mul_f32_e32 v75, 0xbfb8aa3b, v75
	v_exp_f32_e32 v74, v74
	v_exp_f32_e32 v75, v75
	v_cvt_f32_i32_e32 v101, v77
	v_mul_f32_e32 v77, v55, v99
	v_fma_f32 v77, v212, v77, v51
	v_mul_f32_e32 v77, 0xbfb8aa3b, v77
	v_add_f32_e32 v74, 1.0, v74
	v_add_f32_e32 v75, 1.0, v75
	v_exp_f32_e32 v77, v77
	v_rcp_f32_e32 v74, v74
	v_rcp_f32_e32 v75, v75
	s_waitcnt vmcnt(3)
	v_cvt_f32_f16_sdwa v79, v94 dst_sel:DWORD dst_unused:UNUSED_PAD src0_sel:WORD_1
	v_cvt_f32_f16_e32 v78, v94
	v_add_f32_e32 v77, 1.0, v77
	v_rcp_f32_e32 v77, v77
	v_cvt_f32_i32_e32 v80, v80
	v_pk_mul_f32 v[74:75], v[74:75], v[78:79]
	v_cvt_f32_f16_sdwa v79, v96 dst_sel:DWORD dst_unused:UNUSED_PAD src0_sel:WORD_1
	v_cvt_f32_f16_e32 v78, v96
	v_cvt_f32_i32_e32 v81, v81
	v_cvt_f32_f16_sdwa v99, v95 dst_sel:DWORD dst_unused:UNUSED_PAD src0_sel:WORD_1
	v_cvt_f32_f16_e32 v98, v95
	v_pk_mul_f32 v[76:77], v[76:77], v[78:79]
	v_mul_f32_e32 v79, v56, v100
	v_fma_f32 v79, v212, v79, v52
	v_mul_f32_e32 v79, 0xbfb8aa3b, v79
	v_exp_f32_e32 v79, v79
	v_mul_f32_e32 v78, v72, v80
	v_fma_f32 v78, v212, v78, v64
	v_mul_f32_e32 v78, 0xbfb8aa3b, v78
	v_add_f32_e32 v79, 1.0, v79
	v_rcp_f32_e32 v80, v79
	v_mul_f32_e32 v79, v73, v81
	v_mul_f32_e32 v81, v57, v101
	v_fma_f32 v79, v212, v79, v65
	v_fma_f32 v81, v212, v81, v53
	v_mul_f32_e32 v79, 0xbfb8aa3b, v79
	v_mul_f32_e32 v81, 0xbfb8aa3b, v81
	v_exp_f32_e32 v78, v78
	v_exp_f32_e32 v79, v79
	v_exp_f32_e32 v81, v81
	v_cvt_f32_f16_sdwa v95, v97 dst_sel:DWORD dst_unused:UNUSED_PAD src0_sel:WORD_1
	v_add_f32_e32 v78, 1.0, v78
	v_add_f32_e32 v79, 1.0, v79
	v_add_f32_e32 v81, 1.0, v81
	v_rcp_f32_e32 v78, v78
	v_rcp_f32_e32 v79, v79
	v_rcp_f32_e32 v81, v81
	v_cvt_f32_f16_e32 v94, v97
	s_and_b64 vcc, exec, s[36:37]
	v_pk_mul_f32 v[78:79], v[78:79], v[98:99]
	v_pk_mul_f32 v[80:81], v[80:81], v[94:95]
	s_cbranch_vccnz .LBB0_1283
	v_cvt_f32_f16_sdwa v95, v170 dst_sel:DWORD dst_unused:UNUSED_PAD src0_sel:WORD_1
	v_cvt_f32_f16_e32 v94, v170
	s_waitcnt vmcnt(3)
	v_cvt_f32_f16_sdwa v97, v178 dst_sel:DWORD dst_unused:UNUSED_PAD src0_sel:WORD_1
	v_cvt_f32_f16_e32 v96, v178
	v_cvt_f32_f16_sdwa v99, v171 dst_sel:DWORD dst_unused:UNUSED_PAD src0_sel:WORD_1
	v_cvt_f32_f16_e32 v98, v171
	v_cvt_f32_f16_sdwa v101, v179 dst_sel:DWORD dst_unused:UNUSED_PAD src0_sel:WORD_1
	v_cvt_f32_f16_e32 v100, v179
	v_cvt_f32_f16_sdwa v103, v172 dst_sel:DWORD dst_unused:UNUSED_PAD src0_sel:WORD_1
	v_cvt_f32_f16_e32 v102, v172
	v_cvt_f32_f16_sdwa v105, v180 dst_sel:DWORD dst_unused:UNUSED_PAD src0_sel:WORD_1
	v_cvt_f32_f16_e32 v104, v180
	v_cvt_f32_f16_sdwa v109, v173 dst_sel:DWORD dst_unused:UNUSED_PAD src0_sel:WORD_1
	v_cvt_f32_f16_e32 v108, v173
	v_cvt_f32_f16_sdwa v111, v181 dst_sel:DWORD dst_unused:UNUSED_PAD src0_sel:WORD_1
	v_cvt_f32_f16_e32 v110, v181
	v_pk_add_f32 v[94:95], v[96:97], v[94:95]
	v_pk_add_f32 v[96:97], v[100:101], v[98:99]
	v_pk_add_f32 v[98:99], v[104:105], v[102:103]
	v_pk_add_f32 v[100:101], v[110:111], v[108:109]
	v_pk_add_f32 v[74:75], v[74:75], v[94:95]
	v_pk_add_f32 v[78:79], v[78:79], v[96:97]
	v_pk_add_f32 v[76:77], v[76:77], v[98:99]
	v_pk_add_f32 v[80:81], v[80:81], v[100:101]

; __device__ __forceinline__ unsigned pk2h(float lo, float hi) { f32x2 v = {lo, hi}; f16x2 h = __builtin_convertvector(v, f16x2); return __builtin_bit_cast(unsigned, h); }
;     __device__ __forceinline__ void operator()(const f32x4 (&acc)[2][2][4][2], const Unit& u, int wr, int wc, int fr, int fq) const {
;     ...
;             for (int m = 2 * mp; m < 2 * mp + 2; ++m) { const size_t off = offa + (size_t)m * 16 * 1024;
;                 f16x8 za[2], zb[2];
;                 if (br == 2) {
; #pragma unroll
;                     for (int bj = 0; bj < 2; ++bj) { za[bj] = *(const g_f16x8*)(Y + off + bj * HALF); zb[bj] = *(const g_f16x8*)(Y + YSTR + off + bj * HALF); } }
; #pragma unroll
;                 for (int bj = 0; bj < 2; ++bj) {
;                     f32x4 a0 = acc[ai][bj][m][0], a1 = acc[ai][bj][m][1];
;                     if constexpr (I8) { const i32x4 i0 = __builtin_bit_cast(i32x4, a0), i1 = __builtin_bit_cast(i32x4, a1);
;                         a0 = (f32x4){(float)i0.x, (float)i0.y, (float)i0.z, (float)i0.w} * sv[bj][0]; a1 = (f32x4){(float)i1.x, (float)i1.y, (float)i1.z, (float)i1.w} * sv[bj][1]; }
;                     const f32x4 g0 = a0 * rs[ai][m] + bv[bj][0], g1 = a1 * rs[ai][m] + bv[bj][1];
;                     const f16x8 yy = yv[m][bj];
;                     float z[8];
; #pragma unroll
;                     for (int e = 0; e < 4; ++e) { z[e] = (float)yy[e] * __builtin_amdgcn_rcpf(1.f + __builtin_amdgcn_exp2f(-LOG2E * g0[e])); z[4 + e] = (float)yy[4 + e] * __builtin_amdgcn_rcpf(1.f + __builtin_amdgcn_exp2f(-LOG2E * g1[e])); }
;                     if (br == 2) {
; #pragma unroll
;                         for (int e = 0; e < 8; ++e) z[e] += (float)za[bj][e] + (float)zb[bj][e]; }
;                     u32x4 w; w.x = pk2h(z[0], z[1]); w.y = pk2h(z[2], z[3]); w.z = pk2h(z[4], z[5]); w.w = pk2h(z[6], z[7]);
;                     f16* dst = (br == 2) ? merged : Yb;
;                     gst16(dst + off + bj * HALF, w); } } } }
.LBB0_1285:
	v_cvt_f32_i32_e32 v20, v20
	v_cvt_f32_i32_e32 v21, v21
	v_cvt_f32_f16_sdwa v75, v93 dst_sel:DWORD dst_unused:UNUSED_PAD src0_sel:WORD_1
	v_cvt_f32_f16_e32 v74, v93
	v_mul_f32_e32 v20, v32, v20
	v_mul_f32_e32 v21, v33, v21
	v_fma_f32 v20, v212, v20, v28
	v_fma_f32 v21, v212, v21, v29
	v_mul_f32_e32 v20, 0xbfb8aa3b, v20
	v_mul_f32_e32 v21, 0xbfb8aa3b, v21
	v_exp_f32_e32 v20, v20
	v_exp_f32_e32 v21, v21
	s_andn2_b64 vcc, exec, s[46:47]
	v_add_f32_e32 v20, 1.0, v20
	v_add_f32_e32 v21, 1.0, v21
	v_rcp_f32_e32 v20, v20
	v_rcp_f32_e32 v21, v21
	s_nop 0
	v_pk_mul_f32 v[20:21], v[20:21], v[74:75]
	s_cbranch_vccnz .LBB0_1287
	v_cvt_f32_f16_sdwa v75, v174 dst_sel:DWORD dst_unused:UNUSED_PAD src0_sel:WORD_1
	v_cvt_f32_f16_e32 v74, v174
	s_waitcnt vmcnt(3)
	v_cvt_f32_f16_sdwa v77, v224 dst_sel:DWORD dst_unused:UNUSED_PAD src0_sel:WORD_1
	v_cvt_f32_f16_e32 v76, v224
	v_cvt_f32_f16_sdwa v79, v175 dst_sel:DWORD dst_unused:UNUSED_PAD src0_sel:WORD_1
	v_cvt_f32_f16_e32 v78, v175
	v_cvt_f32_f16_sdwa v81, v225 dst_sel:DWORD dst_unused:UNUSED_PAD src0_sel:WORD_1
	v_cvt_f32_f16_e32 v80, v225
	v_cvt_f32_f16_sdwa v91, v176 dst_sel:DWORD dst_unused:UNUSED_PAD src0_sel:WORD_1
	v_cvt_f32_f16_e32 v90, v176
	v_cvt_f32_f16_sdwa v93, v226 dst_sel:DWORD dst_unused:UNUSED_PAD src0_sel:WORD_1
	v_cvt_f32_f16_e32 v92, v226
	v_cvt_f32_f16_sdwa v95, v177 dst_sel:DWORD dst_unused:UNUSED_PAD src0_sel:WORD_1
	v_cvt_f32_f16_e32 v94, v177
	v_cvt_f32_f16_sdwa v97, v227 dst_sel:DWORD dst_unused:UNUSED_PAD src0_sel:WORD_1
	v_cvt_f32_f16_e32 v96, v227
	v_pk_add_f32 v[74:75], v[76:77], v[74:75]
	v_pk_add_f32 v[76:77], v[80:81], v[78:79]
	v_pk_add_f32 v[78:79], v[92:93], v[90:91]
	v_pk_add_f32 v[80:81], v[96:97], v[94:95]
	v_pk_add_f32 v[18:19], v[18:19], v[74:75]
	v_pk_add_f32 v[24:25], v[24:25], v[76:77]
	v_pk_add_f32 v[22:23], v[22:23], v[78:79]
	v_pk_add_f32 v[20:21], v[20:21], v[80:81]

; __device__ __forceinline__ unsigned pk2h(float lo, float hi) { f32x2 v = {lo, hi}; f16x2 h = __builtin_convertvector(v, f16x2); return __builtin_bit_cast(unsigned, h); }
;     __device__ __forceinline__ void operator()(const f32x4 (&acc)[2][2][4][2], const Unit& u, int wr, int wc, int fr, int fq) const {
;     ...
;             for (int m = 2 * mp; m < 2 * mp + 2; ++m) { const size_t off = offa + (size_t)m * 16 * 1024;
;                 f16x8 za[2], zb[2];
;                 if (br == 2) {
; #pragma unroll
;                     for (int bj = 0; bj < 2; ++bj) { za[bj] = *(const g_f16x8*)(Y + off + bj * HALF); zb[bj] = *(const g_f16x8*)(Y + YSTR + off + bj * HALF); } }
; #pragma unroll
;                 for (int bj = 0; bj < 2; ++bj) {
;                     f32x4 a0 = acc[ai][bj][m][0], a1 = acc[ai][bj][m][1];
;                     if constexpr (I8) { const i32x4 i0 = __builtin_bit_cast(i32x4, a0), i1 = __builtin_bit_cast(i32x4, a1);
;                         a0 = (f32x4){(float)i0.x, (float)i0.y, (float)i0.z, (float)i0.w} * sv[bj][0]; a1 = (f32x4){(float)i1.x, (float)i1.y, (float)i1.z, (float)i1.w} * sv[bj][1]; }
;                     const f32x4 g0 = a0 * rs[ai][m] + bv[bj][0], g1 = a1 * rs[ai][m] + bv[bj][1];
;                     const f16x8 yy = yv[m][bj];
;                     float z[8];
; #pragma unroll
;                     for (int e = 0; e < 4; ++e) { z[e] = (float)yy[e] * __builtin_amdgcn_rcpf(1.f + __builtin_amdgcn_exp2f(-LOG2E * g0[e])); z[4 + e] = (float)yy[4 + e] * __builtin_amdgcn_rcpf(1.f + __builtin_amdgcn_exp2f(-LOG2E * g1[e])); }
;                     if (br == 2) {
; #pragma unroll
;                         for (int e = 0; e < 8; ++e) z[e] += (float)za[bj][e] + (float)zb[bj][e]; }
;                     u32x4 w; w.x = pk2h(z[0], z[1]); w.y = pk2h(z[2], z[3]); w.z = pk2h(z[4], z[5]); w.w = pk2h(z[6], z[7]);
;                     f16* dst = (br == 2) ? merged : Yb;
;                     gst16(dst + off + bj * HALF, w); } } } }
.LBB0_1289:
	v_cvt_f32_i32_e32 v14, v14
	v_cvt_f32_i32_e32 v15, v15
	v_cvt_f32_i32_e32 v18, v10
	v_cvt_f32_i32_e32 v19, v12
	v_mul_f32_e32 v10, v70, v14
	v_mul_f32_e32 v12, v71, v15
	v_fma_f32 v10, v213, v10, v62
	v_cvt_f32_i32_e32 v14, v11
	v_fma_f32 v12, v213, v12, v63
	v_mul_f32_e32 v10, 0xbfb8aa3b, v10
	v_mul_f32_e32 v12, 0xbfb8aa3b, v12
	v_exp_f32_e32 v10, v10
	v_exp_f32_e32 v12, v12
	v_mul_f32_e32 v11, v54, v18
	v_fma_f32 v11, v213, v11, v50
	v_mul_f32_e32 v14, v55, v14
	v_mul_f32_e32 v11, 0xbfb8aa3b, v11
	v_fma_f32 v14, v213, v14, v51
	v_add_f32_e32 v10, 1.0, v10
	v_exp_f32_e32 v15, v11
	v_add_f32_e32 v11, 1.0, v12
	v_mul_f32_e32 v14, 0xbfb8aa3b, v14
	v_cvt_f32_i32_e32 v16, v16
	v_cvt_f32_i32_e32 v17, v17
	v_cvt_f32_i32_e32 v20, v13
	v_rcp_f32_e32 v10, v10
	v_rcp_f32_e32 v11, v11
	s_waitcnt vmcnt(3)
	v_cvt_f32_f16_sdwa v13, v86 dst_sel:DWORD dst_unused:UNUSED_PAD src0_sel:WORD_1
	v_cvt_f32_f16_e32 v12, v86
	v_exp_f32_e32 v18, v14
	v_mul_f32_e32 v17, v73, v17
	v_fmac_f32_e32 v65, v213, v17
	v_pk_mul_f32 v[10:11], v[10:11], v[12:13]
	v_add_f32_e32 v12, 1.0, v18
	v_mul_f32_e32 v13, v72, v16
	v_mul_f32_e32 v18, v56, v19
	v_mul_f32_e32 v19, v57, v20
	v_fma_f32 v13, v213, v13, v64
	v_fma_f32 v18, v213, v18, v52
	v_fmac_f32_e32 v53, v213, v19
	v_mul_f32_e32 v13, 0xbfb8aa3b, v13
	v_mul_f32_e32 v18, 0xbfb8aa3b, v18
	v_mul_f32_e32 v17, 0xbfb8aa3b, v65
	v_mul_f32_e32 v19, 0xbfb8aa3b, v53
	v_exp_f32_e32 v16, v13
	v_exp_f32_e32 v18, v18
	v_exp_f32_e32 v17, v17
	v_exp_f32_e32 v19, v19
	v_add_f32_e32 v14, 1.0, v15
	v_add_f32_e32 v16, 1.0, v16
	v_add_f32_e32 v18, 1.0, v18
	v_add_f32_e32 v17, 1.0, v17
	v_add_f32_e32 v19, 1.0, v19
	v_rcp_f32_e32 v14, v14
	v_rcp_f32_e32 v15, v12
	v_cvt_f32_f16_sdwa v13, v88 dst_sel:DWORD dst_unused:UNUSED_PAD src0_sel:WORD_1
	v_cvt_f32_f16_e32 v12, v88
	v_rcp_f32_e32 v16, v16
	v_rcp_f32_e32 v18, v18
	v_rcp_f32_e32 v17, v17
	v_cvt_f32_f16_sdwa v21, v87 dst_sel:DWORD dst_unused:UNUSED_PAD src0_sel:WORD_1
	v_cvt_f32_f16_e32 v20, v87
	v_rcp_f32_e32 v19, v19
	v_cvt_f32_f16_sdwa v23, v89 dst_sel:DWORD dst_unused:UNUSED_PAD src0_sel:WORD_1
	v_cvt_f32_f16_e32 v22, v89
	v_pk_mul_f32 v[12:13], v[14:15], v[12:13]
	v_pk_mul_f32 v[14:15], v[16:17], v[20:21]
	s_and_b64 vcc, exec, s[36:37]
	v_pk_mul_f32 v[16:17], v[18:19], v[22:23]
	s_cbranch_vccnz .LBB0_1291
	v_cvt_f32_f16_sdwa v19, v154 dst_sel:DWORD dst_unused:UNUSED_PAD src0_sel:WORD_1
	v_cvt_f32_f16_e32 v18, v154
	s_waitcnt vmcnt(9)
	v_cvt_f32_f16_sdwa v21, v162 dst_sel:DWORD dst_unused:UNUSED_PAD src0_sel:WORD_1
	v_cvt_f32_f16_e32 v20, v162
	v_cvt_f32_f16_sdwa v23, v155 dst_sel:DWORD dst_unused:UNUSED_PAD src0_sel:WORD_1
	v_cvt_f32_f16_e32 v22, v155
	v_cvt_f32_f16_sdwa v25, v163 dst_sel:DWORD dst_unused:UNUSED_PAD src0_sel:WORD_1
	v_cvt_f32_f16_e32 v24, v163
	v_cvt_f32_f16_sdwa v51, v156 dst_sel:DWORD dst_unused:UNUSED_PAD src0_sel:WORD_1
	v_cvt_f32_f16_e32 v50, v156
	v_cvt_f32_f16_sdwa v53, v164 dst_sel:DWORD dst_unused:UNUSED_PAD src0_sel:WORD_1
	v_cvt_f32_f16_e32 v52, v164
	v_cvt_f32_f16_sdwa v55, v157 dst_sel:DWORD dst_unused:UNUSED_PAD src0_sel:WORD_1
	v_cvt_f32_f16_e32 v54, v157
	v_cvt_f32_f16_sdwa v57, v165 dst_sel:DWORD dst_unused:UNUSED_PAD src0_sel:WORD_1
	v_cvt_f32_f16_e32 v56, v165
	v_pk_add_f32 v[18:19], v[20:21], v[18:19]
	v_pk_add_f32 v[20:21], v[24:25], v[22:23]
	v_pk_add_f32 v[22:23], v[52:53], v[50:51]
	v_pk_add_f32 v[24:25], v[56:57], v[54:55]
	v_pk_add_f32 v[10:11], v[10:11], v[18:19]
	v_pk_add_f32 v[14:15], v[14:15], v[20:21]
	v_pk_add_f32 v[12:13], v[12:13], v[22:23]
	v_pk_add_f32 v[16:17], v[16:17], v[24:25]
; __device__ __forceinline__ unsigned pk2h(float lo, float hi) { f32x2 v = {lo, hi}; f16x2 h = __builtin_convertvector(v, f16x2); return __builtin_bit_cast(unsigned, h); }
;     __device__ __forceinline__ void operator()(const f32x4 (&acc)[2][2][4][2], const Unit& u, int wr, int wc, int fr, int fq) const {
;     ...
;             for (int m = 2 * mp; m < 2 * mp + 2; ++m) { const size_t off = offa + (size_t)m * 16 * 1024;
;                 f16x8 za[2], zb[2];
;                 if (br == 2) {
; #pragma unroll
;                     for (int bj = 0; bj < 2; ++bj) { za[bj] = *(const g_f16x8*)(Y + off + bj * HALF); zb[bj] = *(const g_f16x8*)(Y + YSTR + off + bj * HALF); } }
; #pragma unroll
;                 for (int bj = 0; bj < 2; ++bj) {
;                     f32x4 a0 = acc[ai][bj][m][0], a1 = acc[ai][bj][m][1];
;                     if constexpr (I8) { const i32x4 i0 = __builtin_bit_cast(i32x4, a0), i1 = __builtin_bit_cast(i32x4, a1);
;                         a0 = (f32x4){(float)i0.x, (float)i0.y, (float)i0.z, (float)i0.w} * sv[bj][0]; a1 = (f32x4){(float)i1.x, (float)i1.y, (float)i1.z, (float)i1.w} * sv[bj][1]; }
;                     const f32x4 g0 = a0 * rs[ai][m] + bv[bj][0], g1 = a1 * rs[ai][m] + bv[bj][1];
;                     const f16x8 yy = yv[m][bj];
;                     float z[8];
; #pragma unroll
;                     for (int e = 0; e < 4; ++e) { z[e] = (float)yy[e] * __builtin_amdgcn_rcpf(1.f + __builtin_amdgcn_exp2f(-LOG2E * g0[e])); z[4 + e] = (float)yy[4 + e] * __builtin_amdgcn_rcpf(1.f + __builtin_amdgcn_exp2f(-LOG2E * g1[e])); }
;                     if (br == 2) {
; #pragma unroll
;                         for (int e = 0; e < 8; ++e) z[e] += (float)za[bj][e] + (float)zb[bj][e]; }
;                     u32x4 w; w.x = pk2h(z[0], z[1]); w.y = pk2h(z[2], z[3]); w.z = pk2h(z[4], z[5]); w.w = pk2h(z[6], z[7]);
;                     f16* dst = (br == 2) ? merged : Yb;
;                     gst16(dst + off + bj * HALF, w); } } } }
.LBB0_1291:
	v_cvt_f32_i32_e32 v6, v6
	v_cvt_f32_i32_e32 v7, v7
	s_mov_b32 s26, 0x18000
	v_cvt_pk_f16_f32 v10, v10, v11
	v_cvt_pk_f16_f32 v11, v14, v15
	v_add_co_u32_e32 v14, vcc, s26, v106
	v_cvt_pk_f16_f32 v12, v12, v13
	v_cvt_pk_f16_f32 v13, v16, v17
	v_addc_co_u32_e32 v15, vcc, 0, v107, vcc
	global_store_dwordx4 v[14:15], v[10:13], off
	v_cvt_f32_i32_e32 v8, v8
	v_cvt_f32_i32_e32 v9, v9
	v_cvt_f32_i32_e32 v10, v2
	v_mul_f32_e32 v2, v38, v6
	v_cvt_f32_i32_e32 v11, v4
	v_mul_f32_e32 v4, v39, v7
	v_fma_f32 v2, v213, v2, v34
	v_cvt_f32_i32_e32 v6, v3
	v_fma_f32 v4, v213, v4, v35
	v_mul_f32_e32 v2, 0xbfb8aa3b, v2
	v_mul_f32_e32 v4, 0xbfb8aa3b, v4
	v_exp_f32_e32 v2, v2
	v_exp_f32_e32 v4, v4
	v_mul_f32_e32 v3, v30, v10
	v_fma_f32 v3, v213, v3, v26
	v_mul_f32_e32 v6, v31, v6
	v_mul_f32_e32 v3, 0xbfb8aa3b, v3
	v_fma_f32 v6, v213, v6, v27
	v_add_f32_e32 v2, 1.0, v2
	v_exp_f32_e32 v7, v3
	v_add_f32_e32 v3, 1.0, v4
	v_mul_f32_e32 v6, 0xbfb8aa3b, v6
	v_cvt_f32_i32_e32 v12, v5
	v_rcp_f32_e32 v2, v2
	v_rcp_f32_e32 v3, v3
	s_waitcnt vmcnt(3)
	v_cvt_f32_f16_sdwa v5, v82 dst_sel:DWORD dst_unused:UNUSED_PAD src0_sel:WORD_1
	v_cvt_f32_f16_e32 v4, v82
	v_exp_f32_e32 v10, v6
	v_mul_f32_e32 v9, v41, v9
	v_fmac_f32_e32 v37, v213, v9
	v_pk_mul_f32 v[2:3], v[2:3], v[4:5]
	v_add_f32_e32 v4, 1.0, v10
	v_mul_f32_e32 v5, v40, v8
	v_mul_f32_e32 v10, v32, v11
	v_mul_f32_e32 v11, v33, v12
	v_fma_f32 v5, v213, v5, v36
	v_fma_f32 v10, v213, v10, v28
	v_fmac_f32_e32 v29, v213, v11
	v_mul_f32_e32 v5, 0xbfb8aa3b, v5
	v_mul_f32_e32 v10, 0xbfb8aa3b, v10
	v_mul_f32_e32 v9, 0xbfb8aa3b, v37
	v_mul_f32_e32 v11, 0xbfb8aa3b, v29
	v_exp_f32_e32 v8, v5
	v_exp_f32_e32 v10, v10
	v_exp_f32_e32 v9, v9
	v_exp_f32_e32 v11, v11
	v_add_f32_e32 v6, 1.0, v7
	v_add_f32_e32 v8, 1.0, v8
	v_add_f32_e32 v10, 1.0, v10
	v_add_f32_e32 v9, 1.0, v9
	v_add_f32_e32 v11, 1.0, v11
	v_rcp_f32_e32 v6, v6
	v_rcp_f32_e32 v7, v4
	v_cvt_f32_f16_sdwa v5, v84 dst_sel:DWORD dst_unused:UNUSED_PAD src0_sel:WORD_1
	v_cvt_f32_f16_e32 v4, v84
	v_rcp_f32_e32 v8, v8
	v_rcp_f32_e32 v10, v10
	v_rcp_f32_e32 v9, v9
	v_cvt_f32_f16_sdwa v13, v83 dst_sel:DWORD dst_unused:UNUSED_PAD src0_sel:WORD_1
	v_cvt_f32_f16_e32 v12, v83
	v_rcp_f32_e32 v11, v11
	v_cvt_f32_f16_sdwa v15, v85 dst_sel:DWORD dst_unused:UNUSED_PAD src0_sel:WORD_1
	v_cvt_f32_f16_e32 v14, v85
	v_pk_mul_f32 v[4:5], v[6:7], v[4:5]
	v_pk_mul_f32 v[6:7], v[8:9], v[12:13]
	s_and_b64 vcc, exec, s[36:37]
	v_pk_mul_f32 v[8:9], v[10:11], v[14:15]
	s_cbranch_vccnz .LBB0_1293
	v_cvt_f32_f16_sdwa v11, v158 dst_sel:DWORD dst_unused:UNUSED_PAD src0_sel:WORD_1
	v_cvt_f32_f16_e32 v10, v158
	s_waitcnt vmcnt(9)
	v_cvt_f32_f16_sdwa v13, v166 dst_sel:DWORD dst_unused:UNUSED_PAD src0_sel:WORD_1
	v_cvt_f32_f16_e32 v12, v166
	v_cvt_f32_f16_sdwa v15, v159 dst_sel:DWORD dst_unused:UNUSED_PAD src0_sel:WORD_1
	v_cvt_f32_f16_e32 v14, v159
	v_cvt_f32_f16_sdwa v17, v167 dst_sel:DWORD dst_unused:UNUSED_PAD src0_sel:WORD_1
	v_cvt_f32_f16_e32 v16, v167
	v_cvt_f32_f16_sdwa v19, v160 dst_sel:DWORD dst_unused:UNUSED_PAD src0_sel:WORD_1
	v_cvt_f32_f16_e32 v18, v160
	v_cvt_f32_f16_sdwa v21, v168 dst_sel:DWORD dst_unused:UNUSED_PAD src0_sel:WORD_1
	v_cvt_f32_f16_e32 v20, v168
	v_cvt_f32_f16_sdwa v23, v161 dst_sel:DWORD dst_unused:UNUSED_PAD src0_sel:WORD_1
	v_cvt_f32_f16_e32 v22, v161
	v_cvt_f32_f16_sdwa v25, v169 dst_sel:DWORD dst_unused:UNUSED_PAD src0_sel:WORD_1
	v_cvt_f32_f16_e32 v24, v169
	v_pk_add_f32 v[10:11], v[12:13], v[10:11]
	v_pk_add_f32 v[12:13], v[16:17], v[14:15]
	v_pk_add_f32 v[14:15], v[20:21], v[18:19]
	v_pk_add_f32 v[16:17], v[24:25], v[22:23]
	v_pk_add_f32 v[2:3], v[2:3], v[10:11]
	v_pk_add_f32 v[6:7], v[6:7], v[12:13]
	v_pk_add_f32 v[4:5], v[4:5], v[14:15]
	v_pk_add_f32 v[8:9], v[8:9], v[16:17]
